# deferred weight-conversion split: 3000 + 1500 tiles deferred, idle-slot quotas 6/8/7/8
# speedup vs baseline: 1.0069x; 1.0041x over previous
; __device__ __forceinline__ void bt_load(const float* __restrict__ src, int N, int perm, int it, int ntn, f32x4 (&v)[8]) {
;     const int wid = threadIdx.x >> 6, lane = threadIdx.x & 63;
;     const int per = 16 * ntn, z = it / per, r = it % per, kt = r / ntn, nt = r % ntn;
;     const int np = nt * 256 + lane * 4;
;     const int sc = perm ? (nt * 128 + (lane & 31) * 4 + (lane >> 5) * 1024) : np;
;     const float* p = src + (size_t)z * 1024 * N + (size_t)(kt * 64 + wid * 8) * N + sc;
; #pragma unroll
;     for (int i = 0; i < 8; ++i) v[i] = __builtin_nontemporal_load((const f32x4*)(p + (size_t)i * N));
; }
; __device__ __forceinline__ void ph_big_transpose(const float* __restrict__ src, int N, int perm, int batch, bf16* __restrict__ dst, float* tile  , int G, int ndefer) {
;     const int tid = threadIdx.x, wid = tid >> 6, lane = tid & 63, ntn = N / 256, total = batch * 16 * ntn - ndefer;
;     int it = (int)blockIdx.x;
;     if (it >= total) return;
;     f32x4 cur[8], nxt[8], nx2[8];
;     bt_load(src, N, perm, it, ntn, cur);
;     if (it + G < total) bt_load(src, N, perm, it + G, ntn, nxt);
;     for (; it < total; it += G) {
;         const bool more = it + G < total, more2 = it + 2 * G < total;
;         if (more2) bt_load(src, N, perm, it + 2 * G, ntn, nx2);
.LBB0_63:
	s_cmpk_gt_i32 s2, 0x1447
	s_waitcnt lgkmcnt(0)
	s_barrier
	s_cbranch_scc1 .LBB0_71
	s_ashr_i32 s0, s2, 31
	s_lshr_b32 s0, s0, 25
	s_add_i32 s1, s2, s0
	s_ashr_i32 s0, s1, 7
	s_and_b32 s1, s1, 0xff80
	s_sub_i32 s1, s2, s1
	s_bfe_i32 s4, s1, 0x80000
	s_bfe_u32 s4, s4, 0x3000c
	s_add_i32 s4, s1, s4
	s_bfe_i32 s5, s4, 0x80000
	s_and_b32 s4, s4, 0xf8
	v_lshlrev_b32_e32 v2, 2, v0
	s_sub_i32 s1, s1, s4
	v_and_b32_e32 v2, 0x7c, v2
	v_lshlrev_b32_e32 v3, 5, v0
	s_movk_i32 s4, 0x400
	s_sext_i32_i8 s1, s1
	v_and_or_b32 v99, v3, s4, v2
	v_lshl_add_u32 v2, s1, 7, v99
	s_ashr_i32 s1, s0, 31
	s_lshl_b64 s[0:1], s[0:1], 23
	s_sext_i32_i16 s5, s5
	s_add_u32 s0, s68, s0
	s_addc_u32 s1, s69, s1
	s_lshl_b32 s4, s5, 3
	v_lshrrev_b32_e32 v3, 3, v0
	s_andn2_b32 s4, s4, 63
	v_and_b32_e32 v110, 56, v3
	v_or_b32_e32 v4, s4, v110
	v_ashrrev_i32_e32 v5, 31, v4
	v_lshlrev_b64 v[4:5], 13, v[4:5]
	v_lshl_add_u64 v[4:5], s[0:1], 0, v[4:5]
	v_ashrrev_i32_e32 v3, 31, v2
	v_lshl_add_u64 v[2:3], v[2:3], 2, v[4:5]
	s_movk_i32 s0, 0x2000
	v_add_co_u32_e32 v4, vcc, s0, v2
	s_movk_i32 s1, 0x4000
	s_nop 0
	v_addc_co_u32_e32 v5, vcc, 0, v3, vcc
	global_load_dwordx4 v[38:41], v[2:3], off nt
	global_load_dwordx4 v[34:37], v[4:5], off nt
	v_add_co_u32_e32 v4, vcc, s1, v2
	s_movk_i32 s4, 0x6000
	s_nop 0
	v_addc_co_u32_e32 v5, vcc, 0, v3, vcc
	v_add_co_u32_e32 v6, vcc, s4, v2
	s_mov_b32 s5, 0x8000
	s_nop 0
	v_addc_co_u32_e32 v7, vcc, 0, v3, vcc
	global_load_dwordx4 v[46:49], v[4:5], off nt
	global_load_dwordx4 v[42:45], v[6:7], off nt
	v_add_co_u32_e32 v4, vcc, s5, v2
	s_mov_b32 s6, 0xa000
	s_nop 0
	v_addc_co_u32_e32 v5, vcc, 0, v3, vcc
	v_add_co_u32_e32 v6, vcc, s6, v2
	s_add_i32 s6, s62, s2
	s_nop 0
	v_addc_co_u32_e32 v7, vcc, 0, v3, vcc
	global_load_dwordx4 v[54:57], v[4:5], off nt
	global_load_dwordx4 v[50:53], v[6:7], off nt
	v_add_co_u32_e32 v4, vcc, 0xc000, v2
	s_cmpk_gt_i32 s6, 0x1447
	s_nop 0
	v_addc_co_u32_e32 v5, vcc, 0, v3, vcc
	v_add_co_u32_e32 v2, vcc, 0xe000, v2
	s_nop 1
	v_addc_co_u32_e32 v3, vcc, 0, v3, vcc
	global_load_dwordx4 v[62:65], v[4:5], off nt
	global_load_dwordx4 v[58:61], v[2:3], off nt
	s_cbranch_scc1 .LBB0_66
	s_ashr_i32 s7, s6, 31
	s_lshr_b32 s7, s7, 25
	s_add_i32 s7, s6, s7
	s_ashr_i32 s8, s7, 7
	s_and_b32 s7, s7, 0xff80
	s_sub_i32 s6, s6, s7
	s_bfe_i32 s7, s6, 0x80000
	s_bfe_u32 s7, s7, 0x3000c
	s_add_i32 s7, s6, s7
	s_bfe_i32 s9, s7, 0x80000
	s_and_b32 s7, s7, 0xf8
	s_sub_i32 s6, s6, s7
	s_sext_i32_i16 s10, s9
	s_sext_i32_i8 s6, s6
	s_ashr_i32 s9, s8, 31
	v_lshl_add_u32 v2, s6, 7, v99
	s_lshl_b64 s[6:7], s[8:9], 23
	s_add_u32 s6, s68, s6
	s_addc_u32 s7, s69, s7
	s_lshl_b32 s8, s10, 3
	s_andn2_b32 s8, s8, 63
	v_or_b32_e32 v4, s8, v110
	v_ashrrev_i32_e32 v5, 31, v4
	v_lshlrev_b64 v[4:5], 13, v[4:5]
	v_lshl_add_u64 v[4:5], s[6:7], 0, v[4:5]
	v_ashrrev_i32_e32 v3, 31, v2
	v_lshl_add_u64 v[26:27], v[2:3], 2, v[4:5]
	v_add_co_u32_e32 v6, vcc, s0, v26
	s_nop 1
	v_addc_co_u32_e32 v7, vcc, 0, v27, vcc
	v_add_co_u32_e32 v10, vcc, s1, v26
	global_load_dwordx4 v[2:5], v[26:27], off nt
	s_nop 0
	global_load_dwordx4 v[6:9], v[6:7], off nt
	v_addc_co_u32_e32 v11, vcc, 0, v27, vcc
	v_add_co_u32_e32 v14, vcc, s4, v26
	s_nop 1
	v_addc_co_u32_e32 v15, vcc, 0, v27, vcc
	v_add_co_u32_e32 v18, vcc, s5, v26
	global_load_dwordx4 v[10:13], v[10:11], off nt
	s_nop 0
	global_load_dwordx4 v[14:17], v[14:15], off nt
	v_addc_co_u32_e32 v19, vcc, 0, v27, vcc
	v_add_co_u32_e32 v22, vcc, 0xa000, v26
	s_nop 1
	v_addc_co_u32_e32 v23, vcc, 0, v27, vcc
	v_add_co_u32_e32 v28, vcc, 0xc000, v26
	global_load_dwordx4 v[18:21], v[18:19], off nt
	s_nop 0
	global_load_dwordx4 v[22:25], v[22:23], off nt
	v_addc_co_u32_e32 v29, vcc, 0, v27, vcc
	v_add_co_u32_e32 v30, vcc, 0xe000, v26
	s_nop 1
	v_addc_co_u32_e32 v31, vcc, 0, v27, vcc
	global_load_dwordx4 v[26:29], v[28:29], off nt
	s_nop 0
	global_load_dwordx4 v[30:33], v[30:31], off nt

; __device__ __forceinline__ unsigned g8_cvt_pk(float lo, float hi) { unsigned r; asm volatile("v_cvt_pk_bf16_f32 %0, %1, %2" : "=v"(r) : "v"(lo), "v"(hi)); return r; }
; __device__ __forceinline__ void ph_big_transpose(const float* __restrict__ src, int N, int perm, int batch, bf16* __restrict__ dst, float* tile  , int G, int ndefer) {
;     ...
;     for (; it < total; it += G) {
;         const bool more = it + G < total, more2 = it + 2 * G < total;
;         if (more2) bt_load(src, N, perm, it + 2 * G, ntn, nx2);
;         __syncthreads();
; #pragma unroll
;         for (int i = 0; i < 8; ++i) { float* t = tile + (wid * 8 + i) * 257 + lane * 4; t[0] = cur[i][0]; t[1] = cur[i][1]; t[2] = cur[i][2]; t[3] = cur[i][3]; }
;         __syncthreads();
;         const int per = 16 * ntn, z = it / per, r = it % per, kt = r / ntn, nt = r % ntn;
;         bf16* d = dst + (size_t)z * N * 1024 + (((size_t)nt * 16 + kt) << 14);
;         const int kc = lane & 7;
; #pragma unroll
;         for (int pss = 0; pss < 4; ++pss) {
;             const int n = wid * 32 + pss * 8 + (lane >> 3); float f[8];
; #pragma unroll
;             for (int j = 0; j < 8; ++j) f[j] = tile[(kc * 8 + j) * 257 + n];
;             u32x4 w; w.x = g8_cvt_pk(f[0], f[1]); w.y = g8_cvt_pk(f[2], f[3]); w.z = g8_cvt_pk(f[4], f[5]); w.w = g8_cvt_pk(f[6], f[7]);
;             __builtin_nontemporal_store(w, (u32x4*)(d + n * 64 + kc * 8));
;         }
;         if (more) {
; #pragma unroll
;             for (int i = 0; i < 8; ++i) { cur[i] = nxt[i]; nxt[i] = nx2[i]; } }
;     }
.LBB0_67:
	s_barrier
	s_waitcnt vmcnt(7)
	ds_write_b128 v111, v[38:41]
	v_add_u32_e32 v38, 0x404, v111
	s_ashr_i32 s9, s8, 31
	s_waitcnt vmcnt(6)
	ds_write2_b32 v38, v34, v35 offset1:1
	v_add_u32_e32 v34, 0x40c, v111
	s_lshr_b32 s9, s9, 25
	ds_write2_b32 v34, v36, v37 offset1:1
	v_add_u32_e32 v34, 0x808, v111
	s_add_i32 s9, s8, s9
	s_waitcnt vmcnt(5)
	ds_write2_b64 v34, v[46:47], v[48:49] offset1:1
	v_add_u32_e32 v34, 0xc0c, v111
	s_ashr_i32 s10, s9, 7
	s_and_b32 s9, s9, 0xff80
	s_waitcnt vmcnt(4)
	ds_write2_b32 v34, v42, v43 offset1:1
	v_add_u32_e32 v34, 0xc14, v111
	s_sub_i32 s9, s8, s9
	s_add_i32 s31, s8, s62
	ds_write2_b32 v34, v44, v45 offset1:1
	s_waitcnt vmcnt(3)
	ds_write_b128 v111, v[54:57] offset:4112
	v_add_u32_e32 v34, 0x1414, v111
	s_bfe_i32 s8, s9, 0x80000
	s_waitcnt vmcnt(2)
	ds_write2_b32 v34, v50, v51 offset1:1
	v_add_u32_e32 v34, 0x141c, v111
	s_bfe_u32 s8, s8, 0x3000c
	ds_write2_b32 v34, v52, v53 offset1:1
	v_add_u32_e32 v34, 0x1818, v111
	s_add_i32 s11, s9, s8
	s_waitcnt vmcnt(1)
	ds_write2_b64 v34, v[62:63], v[64:65] offset1:1
	v_add_u32_e32 v34, 0x1c1c, v111
	s_bfe_i32 s8, s11, 0x80000
	s_and_b32 s11, s11, 0xf8
	s_waitcnt vmcnt(0)
	ds_write2_b32 v34, v58, v59 offset1:1
	v_add_u32_e32 v34, 0x1c24, v111
	s_sext_i32_i16 s8, s8
	s_sub_i32 s30, s9, s11
	s_ashr_i32 s11, s10, 31
	ds_write2_b32 v34, v60, v61 offset1:1
	s_waitcnt lgkmcnt(0)
	s_barrier
	s_lshr_b32 s8, s8, 3
	s_lshl_b64 s[10:11], s[10:11], 22
	ds_read_b32 v34, v112 offset:1028
	ds_read_b32 v35, v112 offset:3084
	ds_read_b32 v36, v112 offset:5140
	ds_read_b32 v37, v112 offset:7196
	ds_read_b32 v38, v112 offset:6168
	ds_read_b32 v39, v112 offset:4112
	ds_read_b32 v40, v112 offset:2056
	ds_read_b32 v41, v112
	s_add_u32 s33, s5, s10
	s_addc_u32 s34, s6, s11
	s_bfe_i64 s[10:11], s[30:31], 0x80000
	s_bfe_i64 s[8:9], s[8:9], 0x100000
	s_lshl_b64 s[10:11], s[10:11], 19
	s_add_u32 s10, s33, s10
	s_addc_u32 s11, s34, s11
	s_lshl_b64 s[8:9], s[8:9], 15
	s_waitcnt lgkmcnt(0)
	v_cvt_pk_bf16_f32 v34, v41, v34
	v_cvt_pk_bf16_f32 v35, v40, v35
	v_cvt_pk_bf16_f32 v36, v39, v36
	v_cvt_pk_bf16_f32 v37, v38, v37
	ds_read_b32 v42, v112 offset:1060
	ds_read_b32 v43, v112 offset:3116
	ds_read_b32 v44, v112 offset:5172
	ds_read_b32 v45, v112 offset:7228
	ds_read_b32 v46, v112 offset:6200
	ds_read_b32 v47, v112 offset:4144
	ds_read_b32 v48, v112 offset:2088
	ds_read_b32 v49, v112 offset:32
	s_add_u32 s8, s10, s8
	s_addc_u32 s9, s11, s9
	v_lshl_add_u64 v[38:39], s[8:9], 0, v[100:101]
	v_mov_b32_e32 v103, v101
	v_lshl_add_u64 v[40:41], v[38:39], 0, v[102:103]
	global_store_dwordx4 v[40:41], v[34:37], off nt
	v_mov_b32_e32 v105, v101
	v_lshl_add_u64 v[40:41], v[38:39], 0, v[104:105]
	s_waitcnt lgkmcnt(0)
	v_cvt_pk_bf16_f32 v34, v49, v42
	v_cvt_pk_bf16_f32 v35, v48, v43
	v_cvt_pk_bf16_f32 v36, v47, v44
	v_cvt_pk_bf16_f32 v37, v46, v45
	ds_read_b32 v42, v112 offset:1092
	ds_read_b32 v43, v112 offset:3148
	ds_read_b32 v44, v112 offset:5204
	ds_read_b32 v45, v112 offset:6232
	ds_read_b32 v46, v112 offset:4176
	ds_read_b32 v47, v112 offset:2120
	ds_read_b32 v48, v112 offset:64
	ds_read_b32 v49, v112 offset:7260
	global_store_dwordx4 v[40:41], v[34:37], off nt
	v_mov_b32_e32 v107, v101
	v_lshl_add_u64 v[40:41], v[38:39], 0, v[106:107]
	s_waitcnt lgkmcnt(1)
	v_cvt_pk_bf16_f32 v34, v48, v42
	v_cvt_pk_bf16_f32 v35, v47, v43
	v_cvt_pk_bf16_f32 v36, v46, v44
	s_waitcnt lgkmcnt(0)
	v_cvt_pk_bf16_f32 v37, v45, v49
	ds_read_b32 v42, v112 offset:1124
	ds_read_b32 v43, v112 offset:3180
	ds_read_b32 v44, v112 offset:5236
	ds_read_b32 v45, v112 offset:6264
	ds_read_b32 v46, v112 offset:4208
	ds_read_b32 v47, v112 offset:2152
	ds_read_b32 v48, v112 offset:96
	ds_read_b32 v49, v112 offset:7292
	v_mov_b32_e32 v109, v101
	global_store_dwordx4 v[40:41], v[34:37], off nt
	v_lshl_add_u64 v[38:39], v[38:39], 0, v[108:109]
	v_mov_b64_e32 v[60:61], v[32:33]
	s_waitcnt lgkmcnt(1)
	v_cvt_pk_bf16_f32 v34, v48, v42
	v_cvt_pk_bf16_f32 v35, v47, v43
	v_cvt_pk_bf16_f32 v36, v46, v44
	s_waitcnt lgkmcnt(0)
	v_cvt_pk_bf16_f32 v37, v45, v49
	global_store_dwordx4 v[38:39], v[34:37], off nt
	v_mov_b64_e32 v[64:65], v[28:29]
	v_mov_b64_e32 v[52:53], v[24:25]
	v_mov_b64_e32 v[56:57], v[20:21]
	v_mov_b64_e32 v[44:45], v[16:17]
	v_mov_b64_e32 v[48:49], v[12:13]
	v_mov_b64_e32 v[36:37], v[8:9]
	v_mov_b64_e32 v[40:41], v[4:5]
	v_mov_b64_e32 v[58:59], v[30:31]
	v_mov_b64_e32 v[62:63], v[26:27]
	v_mov_b64_e32 v[50:51], v[22:23]
	v_mov_b64_e32 v[54:55], v[18:19]
	v_mov_b64_e32 v[42:43], v[14:15]
	v_mov_b64_e32 v[46:47], v[10:11]
	v_mov_b64_e32 v[34:35], v[6:7]
	v_mov_b64_e32 v[38:39], v[2:3]
	v_mov_b64_e32 v[30:31], v[94:95]
	v_mov_b64_e32 v[26:27], v[90:91]
	v_mov_b64_e32 v[22:23], v[86:87]
	v_mov_b64_e32 v[18:19], v[82:83]
	v_mov_b64_e32 v[14:15], v[78:79]
	v_mov_b64_e32 v[10:11], v[74:75]
	v_mov_b64_e32 v[6:7], v[70:71]
	v_mov_b64_e32 v[2:3], v[66:67]
	s_cmpk_lt_i32 s31, 0x1448
	v_mov_b64_e32 v[32:33], v[96:97]
	v_mov_b64_e32 v[28:29], v[92:93]
	v_mov_b64_e32 v[24:25], v[88:89]
	v_mov_b64_e32 v[20:21], v[84:85]
	v_mov_b64_e32 v[16:17], v[80:81]
	v_mov_b64_e32 v[12:13], v[76:77]
	v_mov_b64_e32 v[8:9], v[72:73]
	v_mov_b64_e32 v[4:5], v[68:69]
	s_mov_b32 s8, s31
	s_cbranch_scc0 .LBB0_70
; __device__ __forceinline__ void bt_load(const float* __restrict__ src, int N, int perm, int it, int ntn, f32x4 (&v)[8]) {
;     const int wid = threadIdx.x >> 6, lane = threadIdx.x & 63;
;     const int per = 16 * ntn, z = it / per, r = it % per, kt = r / ntn, nt = r % ntn;
;     const int np = nt * 256 + lane * 4;
;     const int sc = perm ? (nt * 128 + (lane & 31) * 4 + (lane >> 5) * 1024) : np;
;     const float* p = src + (size_t)z * 1024 * N + (size_t)(kt * 64 + wid * 8) * N + sc;
; #pragma unroll
;     for (int i = 0; i < 8; ++i) v[i] = __builtin_nontemporal_load((const f32x4*)(p + (size_t)i * N));
; }
; __device__ __forceinline__ void ph_big_transpose(const float* __restrict__ src, int N, int perm, int batch, bf16* __restrict__ dst, float* tile  , int G, int ndefer) {
;     ...
;     for (; it < total; it += G) {
;         const bool more = it + G < total, more2 = it + 2 * G < total;
;         if (more2) bt_load(src, N, perm, it + 2 * G, ntn, nx2);
.LBB0_68:
	s_add_i32 s9, s7, s8
	s_cmpk_gt_i32 s9, 0x1447
	s_cbranch_scc1 .LBB0_67
	s_ashr_i32 s10, s9, 31
	s_lshr_b32 s10, s10, 25
	s_add_i32 s11, s9, s10
	s_ashr_i32 s10, s11, 7
	s_and_b32 s11, s11, 0xff80
	s_sub_i32 s9, s9, s11
	s_bfe_i32 s11, s9, 0x80000
	s_bfe_u32 s11, s11, 0x3000c
	s_add_i32 s11, s9, s11
	s_bfe_i32 s30, s11, 0x80000
	s_and_b32 s11, s11, 0xf8
	s_sub_i32 s9, s9, s11
	s_ashr_i32 s11, s10, 31
	s_lshl_b64 s[10:11], s[10:11], 23
	s_sext_i32_i16 s30, s30
	s_sext_i32_i8 s9, s9
	s_add_u32 s10, s68, s10
	v_lshl_add_u32 v66, s9, 7, v99
	s_addc_u32 s11, s69, s11
	s_lshl_b32 s9, s30, 3
	s_andn2_b32 s9, s9, 63
	v_or_b32_e32 v68, s9, v110
	v_ashrrev_i32_e32 v69, 31, v68
	v_lshlrev_b64 v[68:69], 13, v[68:69]
	v_lshl_add_u64 v[68:69], s[10:11], 0, v[68:69]
	v_ashrrev_i32_e32 v67, 31, v66
	v_lshl_add_u64 v[90:91], v[66:67], 2, v[68:69]
	v_add_co_u32_e32 v70, vcc, s0, v90
	s_nop 1
	v_addc_co_u32_e32 v71, vcc, 0, v91, vcc
	v_add_co_u32_e32 v74, vcc, s1, v90
	global_load_dwordx4 v[66:69], v[90:91], off nt
	s_nop 0
	global_load_dwordx4 v[70:73], v[70:71], off nt
	v_addc_co_u32_e32 v75, vcc, 0, v91, vcc
	v_add_co_u32_e32 v78, vcc, s4, v90
	s_nop 1
	v_addc_co_u32_e32 v79, vcc, 0, v91, vcc
	v_add_co_u32_e32 v82, vcc, 0x8000, v90
	global_load_dwordx4 v[74:77], v[74:75], off nt
	s_nop 0
	global_load_dwordx4 v[78:81], v[78:79], off nt
	v_addc_co_u32_e32 v83, vcc, 0, v91, vcc
	v_add_co_u32_e32 v86, vcc, 0xa000, v90
	s_nop 1
	v_addc_co_u32_e32 v87, vcc, 0, v91, vcc
	v_add_co_u32_e32 v92, vcc, 0xc000, v90
	global_load_dwordx4 v[82:85], v[82:83], off nt
	s_nop 0
	global_load_dwordx4 v[86:89], v[86:87], off nt
	v_addc_co_u32_e32 v93, vcc, 0, v91, vcc
	v_add_co_u32_e32 v94, vcc, 0xe000, v90
	s_nop 1
	v_addc_co_u32_e32 v95, vcc, 0, v91, vcc
	global_load_dwordx4 v[90:93], v[92:93], off nt
	s_nop 0
	global_load_dwordx4 v[94:97], v[94:95], off nt
	s_branch .LBB0_67

; __device__ __forceinline__ void bt_load(const float* __restrict__ src, int N, int perm, int it, int ntn, f32x4 (&v)[8]) {
;     const int wid = threadIdx.x >> 6, lane = threadIdx.x & 63;
;     const int per = 16 * ntn, z = it / per, r = it % per, kt = r / ntn, nt = r % ntn;
;     const int np = nt * 256 + lane * 4;
;     const int sc = perm ? (nt * 128 + (lane & 31) * 4 + (lane >> 5) * 1024) : np;
;     const float* p = src + (size_t)z * 1024 * N + (size_t)(kt * 64 + wid * 8) * N + sc;
; #pragma unroll
;     for (int i = 0; i < 8; ++i) v[i] = __builtin_nontemporal_load((const f32x4*)(p + (size_t)i * N));
; }
; __device__ __forceinline__ void ph_big_transpose(const float* __restrict__ src, int N, int perm, int batch, bf16* __restrict__ dst, float* tile  , int G, int ndefer) {
;     const int tid = threadIdx.x, wid = tid >> 6, lane = tid & 63, ntn = N / 256, total = batch * 16 * ntn - ndefer;
;     int it = (int)blockIdx.x;
;     if (it >= total) return;
;     f32x4 cur[8], nxt[8], nx2[8];
;     bt_load(src, N, perm, it, ntn, cur);
;     if (it + G < total) bt_load(src, N, perm, it + G, ntn, nxt);
;     for (; it < total; it += G) {
;         const bool more = it + G < total, more2 = it + 2 * G < total;
;         if (more2) bt_load(src, N, perm, it + 2 * G, ntn, nx2);
.LBB0_71:
	s_cmpk_gt_i32 s2, 0xa23
	s_cbranch_scc1 .LBB0_79
	s_ashr_i32 s0, s2, 31
	s_lshr_b32 s0, s0, 26
	s_add_i32 s1, s2, s0
	s_ashr_i32 s0, s1, 6
	s_and_b32 s1, s1, 0xffc0
	s_sub_i32 s1, s2, s1
	s_bfe_i32 s4, s1, 0x80000
	s_bfe_u32 s4, s4, 0x2000d
	s_add_i32 s4, s1, s4
	s_bfe_i32 s5, s4, 0x80000
	s_and_b32 s4, s4, 0xfc
	s_sub_i32 s1, s1, s4
	v_lshlrev_b32_e32 v2, 2, v0
	s_sext_i32_i8 s1, s1
	v_and_b32_e32 v99, 0xfc, v2
	v_lshl_or_b32 v2, s1, 8, v99
	s_ashr_i32 s1, s0, 31
	s_lshl_b64 s[0:1], s[0:1], 22
	s_sext_i32_i16 s5, s5
	s_add_u32 s0, s72, s0
	s_addc_u32 s1, s73, s1
	s_lshl_b32 s4, s5, 4
	v_lshrrev_b32_e32 v3, 3, v0
	s_andn2_b32 s4, s4, 63
	v_and_b32_e32 v110, 56, v3
	v_or_b32_e32 v4, s4, v110
	v_ashrrev_i32_e32 v5, 31, v4
	v_lshlrev_b64 v[4:5], 12, v[4:5]
	v_lshl_add_u64 v[4:5], s[0:1], 0, v[4:5]
	v_ashrrev_i32_e32 v3, 31, v2
	v_lshl_add_u64 v[2:3], v[2:3], 2, v[4:5]
	s_movk_i32 s0, 0x2000
	v_add_co_u32_e32 v4, vcc, s0, v2
	s_movk_i32 s4, 0x4000
	s_nop 0
	v_addc_co_u32_e32 v5, vcc, 0, v3, vcc
	global_load_dwordx4 v[42:45], v[4:5], off offset:-4096 nt
	global_load_dwordx4 v[34:37], v[4:5], off nt
	v_add_co_u32_e32 v4, vcc, s4, v2
	s_movk_i32 s1, 0x5000
	s_nop 0
	v_addc_co_u32_e32 v5, vcc, 0, v3, vcc
	global_load_dwordx4 v[46:49], v[4:5], off offset:-4096 nt
	global_load_dwordx4 v[38:41], v[4:5], off nt
	v_add_co_u32_e32 v4, vcc, s1, v2
	s_add_i32 s5, s62, s2
	s_nop 0
	v_addc_co_u32_e32 v5, vcc, 0, v3, vcc
	global_load_dwordx4 v[62:65], v[2:3], off nt
	global_load_dwordx4 v[50:53], v[4:5], off nt
	v_add_co_u32_e32 v4, vcc, 0x6000, v2
	s_cmpk_gt_i32 s5, 0xa23
	s_nop 0
	v_addc_co_u32_e32 v5, vcc, 0, v3, vcc
	v_add_co_u32_e32 v2, vcc, 0x7000, v2
	s_movk_i32 s1, 0x3000
	s_nop 0
	v_addc_co_u32_e32 v3, vcc, 0, v3, vcc
	global_load_dwordx4 v[58:61], v[4:5], off nt
	global_load_dwordx4 v[54:57], v[2:3], off nt
	s_cbranch_scc1 .LBB0_74
	s_ashr_i32 s6, s5, 31
	s_lshr_b32 s6, s6, 26
	s_add_i32 s7, s5, s6
	s_ashr_i32 s6, s7, 6
	s_and_b32 s7, s7, 0xffc0
	s_sub_i32 s5, s5, s7
	s_bfe_i32 s7, s5, 0x80000
	s_bfe_u32 s7, s7, 0x2000d
	s_add_i32 s7, s5, s7
	s_bfe_i32 s8, s7, 0x80000
	s_and_b32 s7, s7, 0xfc
	s_sub_i32 s5, s5, s7
	s_ashr_i32 s7, s6, 31
	s_lshl_b64 s[6:7], s[6:7], 22
	s_sext_i32_i16 s8, s8
	s_sext_i32_i8 s5, s5
	s_add_u32 s6, s72, s6
	v_lshl_or_b32 v2, s5, 8, v99
	s_addc_u32 s7, s73, s7
	s_lshl_b32 s5, s8, 4
	s_andn2_b32 s5, s5, 63
	v_or_b32_e32 v4, s5, v110
	v_ashrrev_i32_e32 v5, 31, v4
	v_lshlrev_b64 v[4:5], 12, v[4:5]
	v_lshl_add_u64 v[4:5], s[6:7], 0, v[4:5]
	v_ashrrev_i32_e32 v3, 31, v2
	v_lshl_add_u64 v[26:27], v[2:3], 2, v[4:5]
	v_add_co_u32_e32 v2, vcc, s0, v26
	s_nop 1
	v_addc_co_u32_e32 v3, vcc, 0, v27, vcc
	v_add_co_u32_e32 v10, vcc, s4, v26
	global_load_dwordx4 v[6:9], v[2:3], off offset:-4096 nt
	s_nop 0
	global_load_dwordx4 v[2:5], v[2:3], off nt
	v_addc_co_u32_e32 v11, vcc, 0, v27, vcc
	v_add_co_u32_e32 v18, vcc, 0x5000, v26
	global_load_dwordx4 v[14:17], v[10:11], off offset:-4096 nt
	s_nop 0
	global_load_dwordx4 v[10:13], v[10:11], off nt
	v_addc_co_u32_e32 v19, vcc, 0, v27, vcc
	v_add_co_u32_e32 v28, vcc, 0x6000, v26
	global_load_dwordx4 v[22:25], v[26:27], off nt
	s_nop 0
	global_load_dwordx4 v[18:21], v[18:19], off nt
	v_addc_co_u32_e32 v29, vcc, 0, v27, vcc
	v_add_co_u32_e32 v30, vcc, 0x7000, v26
	s_nop 1
	v_addc_co_u32_e32 v31, vcc, 0, v27, vcc
	global_load_dwordx4 v[26:29], v[28:29], off nt
	s_nop 0
	global_load_dwordx4 v[30:33], v[30:31], off nt

; __device__ __forceinline__ unsigned g8_cvt_pk(float lo, float hi) { unsigned r; asm volatile("v_cvt_pk_bf16_f32 %0, %1, %2" : "=v"(r) : "v"(lo), "v"(hi)); return r; }
; __device__ __forceinline__ void ph_big_transpose(const float* __restrict__ src, int N, int perm, int batch, bf16* __restrict__ dst, float* tile  , int G, int ndefer) {
;     ...
;     for (; it < total; it += G) {
;         const bool more = it + G < total, more2 = it + 2 * G < total;
;         if (more2) bt_load(src, N, perm, it + 2 * G, ntn, nx2);
;         __syncthreads();
; #pragma unroll
;         for (int i = 0; i < 8; ++i) { float* t = tile + (wid * 8 + i) * 257 + lane * 4; t[0] = cur[i][0]; t[1] = cur[i][1]; t[2] = cur[i][2]; t[3] = cur[i][3]; }
;         __syncthreads();
;         const int per = 16 * ntn, z = it / per, r = it % per, kt = r / ntn, nt = r % ntn;
;         bf16* d = dst + (size_t)z * N * 1024 + (((size_t)nt * 16 + kt) << 14);
;         const int kc = lane & 7;
; #pragma unroll
;         for (int pss = 0; pss < 4; ++pss) {
;             const int n = wid * 32 + pss * 8 + (lane >> 3); float f[8];
; #pragma unroll
;             for (int j = 0; j < 8; ++j) f[j] = tile[(kc * 8 + j) * 257 + n];
;             u32x4 w; w.x = g8_cvt_pk(f[0], f[1]); w.y = g8_cvt_pk(f[2], f[3]); w.z = g8_cvt_pk(f[4], f[5]); w.w = g8_cvt_pk(f[6], f[7]);
;             __builtin_nontemporal_store(w, (u32x4*)(d + n * 64 + kc * 8));
;         }
;         if (more) {
; #pragma unroll
;             for (int i = 0; i < 8; ++i) { cur[i] = nxt[i]; nxt[i] = nx2[i]; } }
;     }
.LBB0_75:
	s_ashr_i32 s8, s3, 31
	s_barrier
	s_waitcnt vmcnt(3)
	ds_write_b128 v111, v[62:65]
	v_add_u32_e32 v62, 0x404, v111
	s_lshr_b32 s8, s8, 26
	ds_write2_b32 v62, v42, v43 offset1:1
	v_add_u32_e32 v42, 0x40c, v111
	s_add_i32 s9, s3, s8
	ds_write2_b32 v42, v44, v45 offset1:1
	v_add_u32_e32 v42, 0x808, v111
	s_ashr_i32 s8, s9, 6
	s_and_b32 s9, s9, 0xffc0
	s_add_i32 s7, s3, s62
	ds_write2_b64 v42, v[34:35], v[36:37] offset1:1
	v_add_u32_e32 v34, 0xc0c, v111
	s_sub_i32 s3, s3, s9
	ds_write2_b32 v34, v46, v47 offset1:1
	v_add_u32_e32 v34, 0xc14, v111
	s_bfe_i32 s9, s3, 0x80000
	ds_write2_b32 v34, v48, v49 offset1:1
	ds_write_b128 v111, v[38:41] offset:4112
	v_add_u32_e32 v34, 0x1414, v111
	s_bfe_u32 s9, s9, 0x2000d
	s_waitcnt vmcnt(2)
	ds_write2_b32 v34, v50, v51 offset1:1
	v_add_u32_e32 v34, 0x141c, v111
	s_add_i32 s9, s3, s9
	ds_write2_b32 v34, v52, v53 offset1:1
	v_add_u32_e32 v34, 0x1818, v111
	s_bfe_i32 s10, s9, 0x80000
	s_and_b32 s9, s9, 0xfc
	s_waitcnt vmcnt(1)
	ds_write2_b64 v34, v[58:59], v[60:61] offset1:1
	v_add_u32_e32 v34, 0x1c1c, v111
	s_sext_i32_i16 s10, s10
	s_sub_i32 s30, s3, s9
	s_ashr_i32 s9, s8, 31
	s_waitcnt vmcnt(0)
	ds_write2_b32 v34, v54, v55 offset1:1
	v_add_u32_e32 v34, 0x1c24, v111
	s_lshr_b32 s10, s10, 2
	s_lshl_b64 s[8:9], s[8:9], 21
	ds_write2_b32 v34, v56, v57 offset1:1
	s_waitcnt lgkmcnt(0)
	s_barrier
	s_add_u32 s3, s4, s8
	ds_read_b32 v34, v112 offset:1028
	ds_read_b32 v35, v112 offset:3084
	ds_read_b32 v36, v112 offset:5140
	ds_read_b32 v37, v112 offset:7196
	ds_read_b32 v38, v112 offset:6168
	ds_read_b32 v39, v112 offset:4112
	ds_read_b32 v40, v112 offset:2056
	ds_read_b32 v41, v112
	s_addc_u32 s31, s5, s9
	s_bfe_i64 s[8:9], s[30:31], 0x80000
	s_bfe_i64 s[10:11], s[10:11], 0x100000
	s_lshl_b64 s[8:9], s[8:9], 19
	s_add_u32 s3, s3, s8
	s_addc_u32 s30, s31, s9
	s_lshl_b64 s[8:9], s[10:11], 15
	s_waitcnt lgkmcnt(0)
	v_cvt_pk_bf16_f32 v34, v41, v34
	v_cvt_pk_bf16_f32 v35, v40, v35
	v_cvt_pk_bf16_f32 v36, v39, v36
	v_cvt_pk_bf16_f32 v37, v38, v37
	ds_read_b32 v42, v112 offset:1060
	ds_read_b32 v43, v112 offset:3116
	ds_read_b32 v44, v112 offset:5172
	ds_read_b32 v45, v112 offset:7228
	ds_read_b32 v46, v112 offset:6200
	ds_read_b32 v47, v112 offset:4144
	ds_read_b32 v48, v112 offset:2088
	ds_read_b32 v49, v112 offset:32
	s_add_u32 s8, s3, s8
	s_addc_u32 s9, s30, s9
	v_lshl_add_u64 v[38:39], s[8:9], 0, v[100:101]
	v_mov_b32_e32 v103, v101
	v_lshl_add_u64 v[40:41], v[38:39], 0, v[102:103]
	global_store_dwordx4 v[40:41], v[34:37], off nt
	v_mov_b32_e32 v105, v101
	v_lshl_add_u64 v[40:41], v[38:39], 0, v[104:105]
	s_waitcnt lgkmcnt(0)
	v_cvt_pk_bf16_f32 v34, v49, v42
	v_cvt_pk_bf16_f32 v35, v48, v43
	v_cvt_pk_bf16_f32 v36, v47, v44
	v_cvt_pk_bf16_f32 v37, v46, v45
	ds_read_b32 v42, v112 offset:1092
	ds_read_b32 v43, v112 offset:3148
	ds_read_b32 v44, v112 offset:5204
	ds_read_b32 v45, v112 offset:6232
	ds_read_b32 v46, v112 offset:4176
	ds_read_b32 v47, v112 offset:2120
	ds_read_b32 v48, v112 offset:64
	ds_read_b32 v49, v112 offset:7260
	global_store_dwordx4 v[40:41], v[34:37], off nt
	v_mov_b32_e32 v107, v101
	v_lshl_add_u64 v[40:41], v[38:39], 0, v[106:107]
	s_waitcnt lgkmcnt(1)
	v_cvt_pk_bf16_f32 v34, v48, v42
	v_cvt_pk_bf16_f32 v35, v47, v43
	v_cvt_pk_bf16_f32 v36, v46, v44
	s_waitcnt lgkmcnt(0)
	v_cvt_pk_bf16_f32 v37, v45, v49
	ds_read_b32 v42, v112 offset:1124
	ds_read_b32 v43, v112 offset:3180
	ds_read_b32 v44, v112 offset:5236
	ds_read_b32 v45, v112 offset:6264
	ds_read_b32 v46, v112 offset:4208
	ds_read_b32 v47, v112 offset:2152
	ds_read_b32 v48, v112 offset:96
	ds_read_b32 v49, v112 offset:7292
	v_mov_b32_e32 v109, v101
	global_store_dwordx4 v[40:41], v[34:37], off nt
	v_lshl_add_u64 v[38:39], v[38:39], 0, v[108:109]
	v_mov_b64_e32 v[56:57], v[32:33]
	s_waitcnt lgkmcnt(1)
	v_cvt_pk_bf16_f32 v34, v48, v42
	v_cvt_pk_bf16_f32 v35, v47, v43
	v_cvt_pk_bf16_f32 v36, v46, v44
	s_waitcnt lgkmcnt(0)
	v_cvt_pk_bf16_f32 v37, v45, v49
	global_store_dwordx4 v[38:39], v[34:37], off nt
	v_mov_b64_e32 v[60:61], v[28:29]
	v_mov_b64_e32 v[52:53], v[20:21]
	v_mov_b64_e32 v[40:41], v[12:13]
	v_mov_b64_e32 v[48:49], v[16:17]
	v_mov_b64_e32 v[36:37], v[4:5]
	v_mov_b64_e32 v[44:45], v[8:9]
	v_mov_b64_e32 v[64:65], v[24:25]
	v_mov_b64_e32 v[54:55], v[30:31]
	v_mov_b64_e32 v[58:59], v[26:27]
	v_mov_b64_e32 v[50:51], v[18:19]
	v_mov_b64_e32 v[38:39], v[10:11]
	v_mov_b64_e32 v[46:47], v[14:15]
	v_mov_b64_e32 v[34:35], v[2:3]
	v_mov_b64_e32 v[42:43], v[6:7]
	v_mov_b64_e32 v[62:63], v[22:23]
	v_mov_b64_e32 v[30:31], v[94:95]
	v_mov_b64_e32 v[26:27], v[90:91]
	v_mov_b64_e32 v[18:19], v[86:87]
	v_mov_b64_e32 v[10:11], v[82:83]
	v_mov_b64_e32 v[14:15], v[74:75]
	v_mov_b64_e32 v[2:3], v[66:67]
	v_mov_b64_e32 v[6:7], v[70:71]
	v_mov_b64_e32 v[22:23], v[78:79]
	s_cmpk_lt_i32 s7, 0xa24
	v_mov_b64_e32 v[32:33], v[96:97]
	v_mov_b64_e32 v[28:29], v[92:93]
	v_mov_b64_e32 v[20:21], v[88:89]
	v_mov_b64_e32 v[12:13], v[84:85]
	v_mov_b64_e32 v[16:17], v[76:77]
	v_mov_b64_e32 v[4:5], v[68:69]
	v_mov_b64_e32 v[8:9], v[72:73]
	v_mov_b64_e32 v[24:25], v[80:81]
	s_mov_b32 s3, s7
	s_cbranch_scc0 .LBB0_78
.LBB0_76:
	s_add_i32 s7, s6, s3
	s_cmpk_gt_i32 s7, 0xa23
	s_cbranch_scc1 .LBB0_75
	s_ashr_i32 s8, s7, 31
	s_lshr_b32 s8, s8, 26
	s_add_i32 s9, s7, s8
	s_ashr_i32 s8, s9, 6
	s_and_b32 s9, s9, 0xffc0
	s_sub_i32 s7, s7, s9
	s_bfe_i32 s9, s7, 0x80000
	s_bfe_u32 s9, s9, 0x2000d
	s_add_i32 s9, s7, s9
	s_bfe_i32 s10, s9, 0x80000
	s_and_b32 s9, s9, 0xfc
	s_sub_i32 s7, s7, s9
	s_ashr_i32 s9, s8, 31
	s_lshl_b64 s[8:9], s[8:9], 22
	s_sext_i32_i16 s10, s10
	s_sext_i32_i8 s7, s7
	s_add_u32 s8, s72, s8
	v_lshl_or_b32 v66, s7, 8, v99
	s_addc_u32 s9, s73, s9
	s_lshl_b32 s7, s10, 4
	s_andn2_b32 s7, s7, 63
	v_or_b32_e32 v68, s7, v110
	v_ashrrev_i32_e32 v69, 31, v68
	v_lshlrev_b64 v[68:69], 12, v[68:69]
	v_lshl_add_u64 v[68:69], s[8:9], 0, v[68:69]
	v_ashrrev_i32_e32 v67, 31, v66
	v_lshl_add_u64 v[90:91], v[66:67], 2, v[68:69]
	v_add_co_u32_e32 v66, vcc, s0, v90
	s_nop 1
	v_addc_co_u32_e32 v67, vcc, 0, v91, vcc
	v_add_co_u32_e32 v74, vcc, s1, v90
	global_load_dwordx4 v[70:73], v[66:67], off offset:-4096 nt
	s_nop 0
	global_load_dwordx4 v[66:69], v[66:67], off nt
	v_addc_co_u32_e32 v75, vcc, 0, v91, vcc
	v_add_co_u32_e32 v82, vcc, 0x4000, v90
	global_load_dwordx4 v[78:81], v[90:91], off nt
	s_nop 0
	global_load_dwordx4 v[74:77], v[74:75], off nt
	v_addc_co_u32_e32 v83, vcc, 0, v91, vcc
	v_add_co_u32_e32 v86, vcc, 0x5000, v90
	s_nop 1
	v_addc_co_u32_e32 v87, vcc, 0, v91, vcc
	v_add_co_u32_e32 v92, vcc, 0x6000, v90
	global_load_dwordx4 v[82:85], v[82:83], off nt
	s_nop 0
	global_load_dwordx4 v[86:89], v[86:87], off nt
	v_addc_co_u32_e32 v93, vcc, 0, v91, vcc
	v_add_co_u32_e32 v94, vcc, 0x7000, v90
	s_nop 1
	v_addc_co_u32_e32 v95, vcc, 0, v91, vcc
	global_load_dwordx4 v[90:93], v[92:93], off nt
	s_nop 0
	global_load_dwordx4 v[94:97], v[94:95], off nt
	s_branch .LBB0_75

; #define SEAM(k) do { if (IN(k) && IN((k) + 1)) xcd_barrier(bar); \
;         if (PROBE_MASK) { const unsigned long long t_ = __builtin_amdgcn_s_memrealtime(); if ((PROBE_MASK >> (k)) & 1u) pr_acc += t_ - pr_t0; pr_t0 = t_; } } while (0)
; __device__ __forceinline__ void convert_deferred(const Ptrs& P, unsigned char* lds, int quota) {
;     const int tid = threadIdx.x, wid = tid >> 6, lane = tid & 63;
;     float* tile = (float*)lds;
;     volatile __attribute__((address_space(3))) int* slot = (volatile __attribute__((address_space(3))) int*)((__attribute__((address_space(3))) unsigned char*)lds + 131072 + 320 + 11000);
;     unsigned* q = (unsigned*)(P.ws + WS_CTL) + CW_DEFQ;
;     for (int n = 0; n < quota; ++n) {
;         __syncthreads();
;         if (tid == 0) *slot = (int)atomicAdd(q, 1u);
;         __syncthreads();
;         const int t = *slot;
;         if (t >= DEF_GU + DEF_DN) break;
;         const bool gu = t < DEF_GU;
;         const float* src = gu ? P.in[34] : P.in[36]; bf16* dst = (bf16*)(P.ws + (gu ? WS_WGU : WS_WDN));
;         const int N = gu ? 2048 : 1024, ntn = N / 256, it = gu ? 2 * NE * 16 * 8 - DEF_GU + t : 2 * NE * 16 * 4 - DEF_DN + (t - DEF_GU);
; __global__ void __launch_bounds__(NT, 2) mega(Args args) {
;     ...
;     if (IN(2)) { g8::DenseOrder S; S.init(H, D, (const bf16*)(ws + WS_WEVIN), D, R, EVEN_IN_P, G, (int)blockIdx.x, 0); g8::EpiStoreBf16 E{Z, EVEN_IN_P};
;         g8::gemm_phase<g8::EpiStoreBf16, g8::DenseOrder, false, true>(LDSP, D, D, S, E);
;         if (IDLE_LAST(68 * 7)) convert_deferred(P, lds, 4); } SEAM(2);
.LBB0_779:
	s_abs_i32 s3, s62
	v_cvt_f32_u32_e32 v2, s3
	s_sub_i32 s4, 0, s3
	s_mov_b32 s5, 0
	v_rcp_iflag_f32_e32 v2, v2
	s_nop 0
	v_mul_f32_e32 v2, 0x4f7ffffe, v2
	v_cvt_u32_f32_e32 v2, v2
	s_nop 0
	v_readfirstlane_b32 s6, v2
	s_mul_i32 s4, s4, s6
	s_mul_hi_u32 s4, s6, s4
	s_add_i32 s6, s6, s4
	s_mul_hi_u32 s4, s6, 0x1dc
	s_mul_i32 s4, s4, s3
	s_sub_i32 s4, 0x1dc, s4
	s_sub_i32 s6, s4, s3
	s_cmp_ge_u32 s4, s3
	s_cselect_b32 s4, s6, s4
	s_sub_i32 s6, s4, s3
	s_cmp_ge_u32 s4, s3
	s_cselect_b32 s3, s6, s4
	s_cmp_eq_u32 s3, 0
	s_cselect_b64 s[6:7], -1, 0
	s_cmp_lt_i32 s2, s3
	s_cselect_b64 s[8:9], -1, 0
	s_or_b64 s[6:7], s[6:7], s[8:9]
	s_and_b64 vcc, exec, s[6:7]
	s_cbranch_vccnz .LBB0_789
	v_and_b32_e32 v2, 0x7c, v155
	v_lshlrev_b32_e32 v3, 5, v0
	s_movk_i32 s3, 0x400
	v_lshrrev_b32_e32 v4, 6, v0
	v_and_or_b32 v12, v3, s3, v2
	v_bfe_u32 v2, v0, 3, 3
	v_lshl_or_b32 v5, v4, 5, v2
	v_lshlrev_b32_e32 v2, 3, v0
	v_lshl_add_u32 v11, v182, 4, 0
	v_and_b32_e32 v2, 56, v2
	v_mul_u32_u24_e32 v16, 0x2020, v4
	v_mov_b32_e32 v3, 0
	v_lshl_add_u32 v27, v5, 2, 0
	v_mul_u32_u24_e32 v28, 0x404, v2
	v_lshlrev_b32_e32 v10, 6, v5
	s_add_i32 s12, 0, 0x22c38
	v_add_u32_e32 v16, v11, v16
	v_and_b32_e32 v13, 0xfc, v155
	v_and_b32_e32 v14, 56, v154
	s_mov_b32 s3, 6
	v_or_b32_e32 v4, 0x200, v10
	v_mov_b32_e32 v5, v3
	v_or_b32_e32 v6, 0x400, v10
	v_mov_b32_e32 v7, v3
	v_or_b32_e32 v8, 0x600, v10
	v_mov_b32_e32 v9, v3
	v_mov_b32_e32 v15, s12
	s_movk_i32 s13, 0x1193
	s_movk_i32 s14, 0x800
	s_mov_b32 s15, 0x1104e000
	s_movk_i32 s16, -404
	v_add_u32_e32 v17, 0x404, v16
	v_add_u32_e32 v18, 0x40c, v16
	v_add_u32_e32 v19, 0x808, v16
	v_add_u32_e32 v20, 0xc0c, v16
	v_add_u32_e32 v21, 0xc14, v16
	v_add_u32_e32 v22, 0x1414, v16
	v_add_u32_e32 v23, 0x141c, v16
	v_add_u32_e32 v24, 0x1818, v16
	v_add_u32_e32 v25, 0x1c1c, v16
	v_add_u32_e32 v26, 0x1c24, v16
	v_lshlrev_b32_e32 v2, 1, v2
	v_add_u32_e32 v27, v27, v28
	v_lshlrev_b32_e32 v10, 1, v10
	s_branch .LBB0_782

; __device__ __forceinline__ unsigned g8_cvt_pk(float lo, float hi) { unsigned r; asm volatile("v_cvt_pk_bf16_f32 %0, %1, %2" : "=v"(r) : "v"(lo), "v"(hi)); return r; }
; __device__ __forceinline__ void convert_deferred(const Ptrs& P, unsigned char* lds, int quota) {
;     ...
;         const int t = *slot;
;         if (t >= DEF_GU + DEF_DN) break;
;         const bool gu = t < DEF_GU;
;         const float* src = gu ? P.in[34] : P.in[36]; bf16* dst = (bf16*)(P.ws + (gu ? WS_WGU : WS_WDN));
;         const int N = gu ? 2048 : 1024, ntn = N / 256, it = gu ? 2 * NE * 16 * 8 - DEF_GU + t : 2 * NE * 16 * 4 - DEF_DN + (t - DEF_GU);
;         f32x4 cur[8];
;         bt_load(src, N, gu ? 1 : 0, it, ntn, cur);
; #pragma unroll
;         for (int i = 0; i < 8; ++i) { float* tp = tile + (wid * 8 + i) * 257 + lane * 4; tp[0] = cur[i][0]; tp[1] = cur[i][1]; tp[2] = cur[i][2]; tp[3] = cur[i][3]; }
;         __syncthreads();
;         const int per = 16 * ntn, z = it / per, r = it % per, kt = r / ntn, nt = r % ntn;
;         bf16* d = dst + (size_t)z * N * 1024 + (((size_t)nt * 16 + kt) << 14);
;         const int kc = lane & 7;
; #pragma unroll
;         for (int pss = 0; pss < 4; ++pss) {
;             const int nn = wid * 32 + pss * 8 + (lane >> 3); float f[8];
; #pragma unroll
;             for (int j = 0; j < 8; ++j) f[j] = tile[(kc * 8 + j) * 257 + nn];
;             u32x4 w; w.x = g8_cvt_pk(f[0], f[1]); w.y = g8_cvt_pk(f[2], f[3]); w.z = g8_cvt_pk(f[4], f[5]); w.w = g8_cvt_pk(f[6], f[7]);
;             *(u32x4*)(d + nn * 64 + kc * 8) = w;
;         }
.LBB0_786:
	s_or_b64 exec, exec, s[6:7]
	s_waitcnt lgkmcnt(0)
	s_barrier
	ds_read_b32 v11, v15
	s_mov_b64 s[6:7], -1
	s_waitcnt lgkmcnt(0)
	v_cmp_lt_i32_e32 vcc, s13, v11
	v_readfirstlane_b32 s4, v11
	s_cbranch_vccnz .LBB0_781
	s_cmpk_gt_i32 s4, 0xbb7
	s_cselect_b64 vcc, -1, 0
	s_and_b64 s[6:7], vcc, exec
	s_cselect_b32 s6, s15, 0x104e000
	s_cselect_b32 s11, 0x400, s14
	s_cselect_b32 s17, s73, s69
	s_cselect_b32 s20, s72, s68
	s_cselect_b32 s7, s16, 0x1448
	s_cselect_b32 s18, 20, 21
	s_cselect_b32 s21, 10, 11
	s_add_u32 s26, s78, s6
	s_addc_u32 s27, s79, 0
	s_lshr_b32 s8, s11, 4
	s_abs_i32 s6, s8
	v_cvt_f32_u32_e32 v11, s6
	s_sub_i32 s19, 0, s6
	s_add_i32 s7, s7, s4
	s_abs_i32 s9, s7
	v_rcp_iflag_f32_e32 v11, v11
	s_xor_b32 s4, s7, s8
	s_lshr_b32 s10, s11, 8
	s_ashr_i32 s4, s4, 31
	v_mul_f32_e32 v11, 0x4f7ffffe, v11
	v_cvt_u32_f32_e32 v11, v11
	s_nop 0
	v_readfirstlane_b32 s28, v11
	s_mul_i32 s19, s19, s28
	s_mul_hi_u32 s19, s28, s19
	s_add_i32 s28, s28, s19
	s_mul_hi_u32 s19, s9, s28
	s_mul_i32 s28, s19, s6
	s_sub_i32 s9, s9, s28
	s_add_i32 s28, s19, 1
	s_sub_i32 s29, s9, s6
	s_cmp_ge_u32 s9, s6
	s_cselect_b32 s19, s28, s19
	s_cselect_b32 s9, s29, s9
	s_add_i32 s28, s19, 1
	s_cmp_ge_u32 s9, s6
	s_cselect_b32 s6, s28, s19
	s_xor_b32 s6, s6, s4
	s_sub_i32 s6, s6, s4
	s_sext_i32_i8 s4, s10
	v_cvt_f32_i32_e32 v11, s4
	s_mul_i32 s8, s6, s8
	s_sub_i32 s7, s7, s8
	v_cvt_f32_i32_e32 v28, s7
	v_rcp_iflag_f32_e32 v29, v11
	s_xor_b32 s4, s7, s4
	s_ashr_i32 s4, s4, 30
	s_or_b32 s4, s4, 1
	v_mul_f32_e32 v29, v28, v29
	v_trunc_f32_e32 v29, v29
	v_fma_f32 v28, -v29, v11, v28
	v_cvt_i32_f32_e32 v29, v29
	v_cmp_ge_f32_e64 s[8:9], |v28|, |v11|
	s_and_b64 s[8:9], s[8:9], exec
	s_cselect_b32 s4, s4, 0
	v_readfirstlane_b32 s8, v29
	s_add_i32 s8, s8, s4
	s_mul_i32 s9, s8, s10
	s_sub_i32 s10, s7, s9
	s_sext_i32_i8 s7, s10
	v_lshl_add_u32 v11, s7, 7, v12
	v_lshl_or_b32 v28, s7, 8, v13
	s_ashr_i32 s7, s6, 31
	s_sext_i32_i8 s4, s8
	s_lshl_b64 s[18:19], s[6:7], s18
	v_lshl_or_b32 v30, s4, 6, v14
	s_lshl_b64 s[18:19], s[18:19], 2
	v_ashrrev_i32_e32 v31, 31, v30
	s_add_u32 s18, s20, s18
	v_cndmask_b32_e32 v28, v11, v28, vcc
	s_addc_u32 s19, s17, s19
	v_lshlrev_b64 v[30:31], s21, v[30:31]
	v_lshl_add_u64 v[30:31], v[30:31], 2, s[18:19]
	v_ashrrev_i32_e32 v29, 31, v28
	v_lshl_add_u64 v[52:53], v[28:29], 2, v[30:31]
	s_lshl_b64 s[18:19], 12, s21
	s_lshl_b32 s4, s11, 2
	v_lshl_add_u64 v[40:41], v[52:53], 0, s[18:19]
	s_lshl_b64 s[18:19], 24, s21
	v_lshl_add_u64 v[36:37], v[52:53], 0, s[4:5]
	v_lshl_add_u64 v[44:45], v[52:53], 0, s[18:19]
	s_lshl_b64 s[18:19], 28, s21
	v_lshl_add_u64 v[54:55], v[36:37], 0, s[4:5]
	v_lshl_add_u64 v[48:49], v[52:53], 0, s[18:19]
	s_lshl_b32 s4, s11, 3
	s_lshl_b64 s[18:19], 20, s21
	global_load_dwordx4 v[28:31], v[52:53], off nt
	global_load_dwordx4 v[32:35], v[36:37], off nt
	s_nop 0
	global_load_dwordx4 v[36:39], v[54:55], off nt
	s_nop 0
	global_load_dwordx4 v[40:43], v[40:41], off nt
	v_lshl_add_u64 v[54:55], v[54:55], 0, s[4:5]
	v_lshl_add_u64 v[56:57], v[52:53], 0, s[18:19]
	global_load_dwordx4 v[44:47], v[44:45], off nt
	s_nop 0
	global_load_dwordx4 v[48:51], v[48:49], off nt
	s_nop 0
	global_load_dwordx4 v[52:55], v[54:55], off nt
	s_nop 0
	global_load_dwordx4 v[56:59], v[56:57], off nt
	s_lshl_b64 s[6:7], s[6:7], s21
	s_lshl_b64 s[6:7], s[6:7], 11
	s_add_u32 s4, s26, s6
	s_addc_u32 s11, s27, s7
	s_bfe_i64 s[6:7], s[10:11], 0x80000
	s_bfe_i64 s[8:9], s[8:9], 0x80000
	s_lshl_b64 s[6:7], s[6:7], 19
	s_add_u32 s4, s4, s6
	s_addc_u32 s10, s11, s7
	s_lshl_b64 s[6:7], s[8:9], 15
	s_add_u32 s6, s4, s6
	s_addc_u32 s7, s10, s7
	v_mov_b32_e32 v11, v3
	s_add_i32 s3, s3, -1
	s_cmp_eq_u32 s3, 0
	s_waitcnt vmcnt(7)
	ds_write_b128 v16, v[28:31]
	s_waitcnt vmcnt(6)
	ds_write2_b32 v17, v32, v33 offset1:1
	ds_write2_b32 v18, v34, v35 offset1:1
	s_waitcnt vmcnt(3)
	ds_write2_b64 v24, v[44:45], v[46:47] offset1:1
	s_waitcnt vmcnt(2)
	ds_write2_b32 v25, v48, v49 offset1:1
	ds_write2_b32 v26, v50, v51 offset1:1
	ds_write2_b64 v19, v[36:37], v[38:39] offset1:1
	ds_write2_b32 v20, v40, v41 offset1:1
	ds_write2_b32 v21, v42, v43 offset1:1
	s_waitcnt vmcnt(1)
	ds_write_b128 v16, v[52:55] offset:4112
	s_waitcnt vmcnt(0)
	ds_write2_b32 v22, v56, v57 offset1:1
	ds_write2_b32 v23, v58, v59 offset1:1
	s_waitcnt lgkmcnt(0)
	s_barrier
	ds_read_b32 v28, v27 offset:1028
	ds_read_b32 v29, v27 offset:3084
	ds_read_b32 v30, v27 offset:5140
	ds_read_b32 v31, v27 offset:7196
	ds_read_b32 v32, v27 offset:6168
	ds_read_b32 v33, v27 offset:4112
	ds_read_b32 v34, v27 offset:2056
	ds_read_b32 v35, v27
	s_waitcnt lgkmcnt(0)
	v_cvt_pk_bf16_f32 v28, v35, v28
	v_cvt_pk_bf16_f32 v29, v34, v29
	v_cvt_pk_bf16_f32 v30, v33, v30
	v_cvt_pk_bf16_f32 v31, v32, v31
	ds_read_b32 v36, v27 offset:1060
	ds_read_b32 v37, v27 offset:3116
	ds_read_b32 v38, v27 offset:5172
	ds_read_b32 v39, v27 offset:7228
	ds_read_b32 v40, v27 offset:6200
	ds_read_b32 v41, v27 offset:4144
	ds_read_b32 v42, v27 offset:2088
	ds_read_b32 v43, v27 offset:32
	v_lshl_add_u64 v[32:33], s[6:7], 0, v[2:3]
	v_lshl_add_u64 v[34:35], v[32:33], 0, v[10:11]
	global_store_dwordx4 v[34:35], v[28:31], off
	v_lshl_add_u64 v[34:35], v[4:5], 1, v[32:33]
	s_cselect_b64 s[6:7], -1, 0
	s_waitcnt lgkmcnt(0)
	v_cvt_pk_bf16_f32 v28, v43, v36
	v_cvt_pk_bf16_f32 v29, v42, v37
	v_cvt_pk_bf16_f32 v30, v41, v38
	v_cvt_pk_bf16_f32 v31, v40, v39
	ds_read_b32 v11, v27 offset:1092
	ds_read_b32 v36, v27 offset:3148
	ds_read_b32 v37, v27 offset:6232
	ds_read_b32 v38, v27 offset:4176
	ds_read_b32 v39, v27 offset:2120
	ds_read_b32 v40, v27 offset:64
	ds_read_b32 v41, v27 offset:5204
	ds_read_b32 v42, v27 offset:7260
	global_store_dwordx4 v[34:35], v[28:31], off
	v_lshl_add_u64 v[34:35], v[6:7], 1, v[32:33]
	v_lshl_add_u64 v[32:33], v[8:9], 1, v[32:33]
	s_waitcnt lgkmcnt(2)
	v_cvt_pk_bf16_f32 v28, v40, v11
	v_cvt_pk_bf16_f32 v29, v39, v36
	s_waitcnt lgkmcnt(1)
	v_cvt_pk_bf16_f32 v30, v38, v41
	s_waitcnt lgkmcnt(0)
	v_cvt_pk_bf16_f32 v31, v37, v42
	ds_read_b32 v11, v27 offset:1124
	ds_read_b32 v36, v27 offset:3180
	ds_read_b32 v37, v27 offset:6264
	ds_read_b32 v38, v27 offset:4208
	ds_read_b32 v39, v27 offset:2152
	ds_read_b32 v40, v27 offset:96
	ds_read_b32 v41, v27 offset:5236
	ds_read_b32 v42, v27 offset:7292
	global_store_dwordx4 v[34:35], v[28:31], off
	s_waitcnt lgkmcnt(2)
	s_nop 0
	v_cvt_pk_bf16_f32 v28, v40, v11
	v_cvt_pk_bf16_f32 v29, v39, v36
	s_waitcnt lgkmcnt(1)
	v_cvt_pk_bf16_f32 v30, v38, v41
	s_waitcnt lgkmcnt(0)
	v_cvt_pk_bf16_f32 v31, v37, v42
	global_store_dwordx4 v[32:33], v[28:31], off
	s_branch .LBB0_781

; #define SEAM(k) do { if (IN(k) && IN((k) + 1)) xcd_barrier(bar); \
;         if (PROBE_MASK) { const unsigned long long t_ = __builtin_amdgcn_s_memrealtime(); if ((PROBE_MASK >> (k)) & 1u) pr_acc += t_ - pr_t0; pr_t0 = t_; } } while (0)
; __device__ __forceinline__ void convert_deferred(const Ptrs& P, unsigned char* lds, int quota) {
;     const int tid = threadIdx.x, wid = tid >> 6, lane = tid & 63;
;     float* tile = (float*)lds;
;     volatile __attribute__((address_space(3))) int* slot = (volatile __attribute__((address_space(3))) int*)((__attribute__((address_space(3))) unsigned char*)lds + 131072 + 320 + 11000);
;     unsigned* q = (unsigned*)(P.ws + WS_CTL) + CW_DEFQ;
;     for (int n = 0; n < quota; ++n) {
;         __syncthreads();
;         if (tid == 0) *slot = (int)atomicAdd(q, 1u);
;         __syncthreads();
;         const int t = *slot;
;         if (t >= DEF_GU + DEF_DN) break;
;         const bool gu = t < DEF_GU;
;         const float* src = gu ? P.in[34] : P.in[36]; bf16* dst = (bf16*)(P.ws + (gu ? WS_WGU : WS_WDN));
;         const int N = gu ? 2048 : 1024, ntn = N / 256, it = gu ? 2 * NE * 16 * 8 - DEF_GU + t : 2 * NE * 16 * 4 - DEF_DN + (t - DEF_GU);
; __global__ void __launch_bounds__(NT, 2) mega(Args args) {
;     ...
;     if (IN(6)) { g8::DenseOrder S; S.init(MIX, D, (const bf16*)(ws + WS_WEVOUT), D, R, D, G, (int)blockIdx.x, 0); g8::EpiOut E{P, 0};
;         g8::gemm_phase<g8::EpiOut, g8::DenseOrder, false, true>(LDSP, D, D, S, E);
;         if (IDLE_LAST(68 * 4)) convert_deferred(P, lds, 4); } SEAM(6);
.LBB0_1286:
	s_abs_i32 s3, s62
	v_cvt_f32_u32_e32 v2, s3
	s_sub_i32 s4, 0, s3
	s_mov_b32 s5, 0
	v_rcp_iflag_f32_e32 v2, v2
	s_nop 0
	v_mul_f32_e32 v2, 0x4f7ffffe, v2
	v_cvt_u32_f32_e32 v2, v2
	s_nop 0
	v_readfirstlane_b32 s6, v2
	s_mul_i32 s4, s4, s6
	s_mul_hi_u32 s4, s6, s4
	s_add_i32 s6, s6, s4
	s_mul_hi_u32 s4, s6, 0x110
	s_mul_i32 s4, s4, s3
	s_sub_i32 s4, 0x110, s4
	s_sub_i32 s6, s4, s3
	s_cmp_ge_u32 s4, s3
	s_cselect_b32 s4, s6, s4
	s_sub_i32 s6, s4, s3
	s_cmp_ge_u32 s4, s3
	s_cselect_b32 s3, s6, s4
	s_cmp_eq_u32 s3, 0
	s_cselect_b64 s[6:7], -1, 0
	s_cmp_lt_i32 s2, s3
	s_cselect_b64 s[8:9], -1, 0
	s_or_b64 s[6:7], s[6:7], s[8:9]
	s_and_b64 vcc, exec, s[6:7]
	s_cbranch_vccnz .LBB0_1296
	v_and_b32_e32 v2, 0x7c, v188
	v_lshlrev_b32_e32 v3, 5, v0
	s_movk_i32 s3, 0x400
	v_and_or_b32 v12, v3, s3, v2
	v_bfe_u32 v2, v0, 3, 3
	v_lshl_or_b32 v4, v1, 5, v2
	v_lshlrev_b32_e32 v2, 3, v0
	v_lshl_add_u32 v11, v182, 4, 0
	v_and_b32_e32 v2, 56, v2
	v_mul_u32_u24_e32 v16, 0x2020, v1
	v_mov_b32_e32 v3, 0
	v_lshl_add_u32 v27, v4, 2, 0
	v_mul_u32_u24_e32 v28, 0x404, v2
	v_lshlrev_b32_e32 v10, 6, v4
	s_add_i32 s12, 0, 0x22c38
	v_add_u32_e32 v16, v11, v16
	v_and_b32_e32 v13, 0xfc, v188
	v_and_b32_e32 v14, 56, v185
	s_mov_b32 s3, 8
	v_or_b32_e32 v4, 0x200, v10
	v_mov_b32_e32 v5, v3
	v_or_b32_e32 v6, 0x400, v10
	v_mov_b32_e32 v7, v3
	v_or_b32_e32 v8, 0x600, v10
	v_mov_b32_e32 v9, v3
	v_mov_b32_e32 v15, s12
	s_movk_i32 s13, 0x1193
	s_movk_i32 s14, 0x800
	s_mov_b32 s15, 0x1104e000
	s_movk_i32 s16, -404
	v_add_u32_e32 v17, 0x404, v16
	v_add_u32_e32 v18, 0x40c, v16
	v_add_u32_e32 v19, 0x808, v16
	v_add_u32_e32 v20, 0xc0c, v16
	v_add_u32_e32 v21, 0xc14, v16
	v_add_u32_e32 v22, 0x1414, v16
	v_add_u32_e32 v23, 0x141c, v16
	v_add_u32_e32 v24, 0x1818, v16
	v_add_u32_e32 v25, 0x1c1c, v16
	v_add_u32_e32 v26, 0x1c24, v16
	v_lshlrev_b32_e32 v2, 1, v2
	v_add_u32_e32 v27, v27, v28
	v_lshlrev_b32_e32 v10, 1, v10
	s_branch .LBB0_1289

; __device__ __forceinline__ unsigned g8_cvt_pk(float lo, float hi) { unsigned r; asm volatile("v_cvt_pk_bf16_f32 %0, %1, %2" : "=v"(r) : "v"(lo), "v"(hi)); return r; }
; __device__ __forceinline__ void convert_deferred(const Ptrs& P, unsigned char* lds, int quota) {
;     ...
;         const int t = *slot;
;         if (t >= DEF_GU + DEF_DN) break;
;         const bool gu = t < DEF_GU;
;         const float* src = gu ? P.in[34] : P.in[36]; bf16* dst = (bf16*)(P.ws + (gu ? WS_WGU : WS_WDN));
;         const int N = gu ? 2048 : 1024, ntn = N / 256, it = gu ? 2 * NE * 16 * 8 - DEF_GU + t : 2 * NE * 16 * 4 - DEF_DN + (t - DEF_GU);
;         f32x4 cur[8];
;         bt_load(src, N, gu ? 1 : 0, it, ntn, cur);
; #pragma unroll
;         for (int i = 0; i < 8; ++i) { float* tp = tile + (wid * 8 + i) * 257 + lane * 4; tp[0] = cur[i][0]; tp[1] = cur[i][1]; tp[2] = cur[i][2]; tp[3] = cur[i][3]; }
;         __syncthreads();
;         const int per = 16 * ntn, z = it / per, r = it % per, kt = r / ntn, nt = r % ntn;
;         bf16* d = dst + (size_t)z * N * 1024 + (((size_t)nt * 16 + kt) << 14);
;         const int kc = lane & 7;
; #pragma unroll
;         for (int pss = 0; pss < 4; ++pss) {
;             const int nn = wid * 32 + pss * 8 + (lane >> 3); float f[8];
; #pragma unroll
;             for (int j = 0; j < 8; ++j) f[j] = tile[(kc * 8 + j) * 257 + nn];
;             u32x4 w; w.x = g8_cvt_pk(f[0], f[1]); w.y = g8_cvt_pk(f[2], f[3]); w.z = g8_cvt_pk(f[4], f[5]); w.w = g8_cvt_pk(f[6], f[7]);
;             *(u32x4*)(d + nn * 64 + kc * 8) = w;
;         }
.LBB0_1293:
	s_or_b64 exec, exec, s[6:7]
	s_waitcnt lgkmcnt(0)
	s_barrier
	ds_read_b32 v11, v15
	s_mov_b64 s[6:7], -1
	s_waitcnt lgkmcnt(0)
	v_cmp_lt_i32_e32 vcc, s13, v11
	v_readfirstlane_b32 s4, v11
	s_cbranch_vccnz .LBB0_1288
	s_cmpk_gt_i32 s4, 0xbb7
	s_cselect_b64 vcc, -1, 0
	s_and_b64 s[6:7], vcc, exec
	s_cselect_b32 s6, s15, 0x104e000
	s_cselect_b32 s11, 0x400, s14
	s_cselect_b32 s17, s73, s69
	s_cselect_b32 s20, s72, s68
	s_cselect_b32 s7, s16, 0x1448
	s_cselect_b32 s18, 20, 21
	s_cselect_b32 s21, 10, 11
	s_add_u32 s22, s78, s6
	s_addc_u32 s23, s79, 0
	s_lshr_b32 s8, s11, 4
	s_abs_i32 s6, s8
	v_cvt_f32_u32_e32 v11, s6
	s_sub_i32 s19, 0, s6
	s_add_i32 s7, s7, s4
	s_abs_i32 s9, s7
	v_rcp_iflag_f32_e32 v11, v11
	s_xor_b32 s4, s7, s8
	s_lshr_b32 s10, s11, 8
	s_ashr_i32 s4, s4, 31
	v_mul_f32_e32 v11, 0x4f7ffffe, v11
	v_cvt_u32_f32_e32 v11, v11
	s_nop 0
	v_readfirstlane_b32 s24, v11
	s_mul_i32 s19, s19, s24
	s_mul_hi_u32 s19, s24, s19
	s_add_i32 s24, s24, s19
	s_mul_hi_u32 s19, s9, s24
	s_mul_i32 s24, s19, s6
	s_sub_i32 s9, s9, s24
	s_add_i32 s24, s19, 1
	s_sub_i32 s25, s9, s6
	s_cmp_ge_u32 s9, s6
	s_cselect_b32 s19, s24, s19
	s_cselect_b32 s9, s25, s9
	s_add_i32 s24, s19, 1
	s_cmp_ge_u32 s9, s6
	s_cselect_b32 s6, s24, s19
	s_xor_b32 s6, s6, s4
	s_sub_i32 s6, s6, s4
	s_sext_i32_i8 s4, s10
	v_cvt_f32_i32_e32 v11, s4
	s_mul_i32 s8, s6, s8
	s_sub_i32 s7, s7, s8
	v_cvt_f32_i32_e32 v28, s7
	v_rcp_iflag_f32_e32 v29, v11
	s_xor_b32 s4, s7, s4
	s_ashr_i32 s4, s4, 30
	s_or_b32 s4, s4, 1
	v_mul_f32_e32 v29, v28, v29
	v_trunc_f32_e32 v29, v29
	v_fma_f32 v28, -v29, v11, v28
	v_cvt_i32_f32_e32 v29, v29
	v_cmp_ge_f32_e64 s[8:9], |v28|, |v11|
	s_and_b64 s[8:9], s[8:9], exec
	s_cselect_b32 s4, s4, 0
	v_readfirstlane_b32 s8, v29
	s_add_i32 s8, s8, s4
	s_mul_i32 s9, s8, s10
	s_sub_i32 s10, s7, s9
	s_sext_i32_i8 s7, s10
	v_lshl_add_u32 v11, s7, 7, v12
	v_lshl_or_b32 v28, s7, 8, v13
	s_ashr_i32 s7, s6, 31
	s_sext_i32_i8 s4, s8
	s_lshl_b64 s[18:19], s[6:7], s18
	v_lshl_or_b32 v30, s4, 6, v14
	s_lshl_b64 s[18:19], s[18:19], 2
	v_ashrrev_i32_e32 v31, 31, v30
	s_add_u32 s18, s20, s18
	v_cndmask_b32_e32 v28, v11, v28, vcc
	s_addc_u32 s19, s17, s19
	v_lshlrev_b64 v[30:31], s21, v[30:31]
	v_lshl_add_u64 v[30:31], v[30:31], 2, s[18:19]
	v_ashrrev_i32_e32 v29, 31, v28
	v_lshl_add_u64 v[52:53], v[28:29], 2, v[30:31]
	s_lshl_b64 s[18:19], 12, s21
	s_lshl_b32 s4, s11, 2
	v_lshl_add_u64 v[40:41], v[52:53], 0, s[18:19]
	s_lshl_b64 s[18:19], 24, s21
	v_lshl_add_u64 v[36:37], v[52:53], 0, s[4:5]
	v_lshl_add_u64 v[44:45], v[52:53], 0, s[18:19]
	s_lshl_b64 s[18:19], 28, s21
	v_lshl_add_u64 v[54:55], v[36:37], 0, s[4:5]
	v_lshl_add_u64 v[48:49], v[52:53], 0, s[18:19]
	s_lshl_b32 s4, s11, 3
	s_lshl_b64 s[18:19], 20, s21
	global_load_dwordx4 v[28:31], v[52:53], off nt
	global_load_dwordx4 v[32:35], v[36:37], off nt
	s_nop 0
	global_load_dwordx4 v[36:39], v[54:55], off nt
	s_nop 0
	global_load_dwordx4 v[40:43], v[40:41], off nt
	v_lshl_add_u64 v[54:55], v[54:55], 0, s[4:5]
	v_lshl_add_u64 v[56:57], v[52:53], 0, s[18:19]
	global_load_dwordx4 v[44:47], v[44:45], off nt
	s_nop 0
	global_load_dwordx4 v[48:51], v[48:49], off nt
	s_nop 0
	global_load_dwordx4 v[52:55], v[54:55], off nt
	s_nop 0
	global_load_dwordx4 v[56:59], v[56:57], off nt
	s_lshl_b64 s[6:7], s[6:7], s21
	s_lshl_b64 s[6:7], s[6:7], 11
	s_add_u32 s4, s22, s6
	s_addc_u32 s11, s23, s7
	s_bfe_i64 s[6:7], s[10:11], 0x80000
	s_bfe_i64 s[8:9], s[8:9], 0x80000
	s_lshl_b64 s[6:7], s[6:7], 19
	s_add_u32 s4, s4, s6
	s_addc_u32 s10, s11, s7
	s_lshl_b64 s[6:7], s[8:9], 15
	s_add_u32 s6, s4, s6
	s_addc_u32 s7, s10, s7
	v_mov_b32_e32 v11, v3
	s_add_i32 s3, s3, -1
	s_cmp_eq_u32 s3, 0
	s_waitcnt vmcnt(7)
	ds_write_b128 v16, v[28:31]
	s_waitcnt vmcnt(6)
	ds_write2_b32 v17, v32, v33 offset1:1
	ds_write2_b32 v18, v34, v35 offset1:1
	s_waitcnt vmcnt(3)
	ds_write2_b64 v24, v[44:45], v[46:47] offset1:1
	s_waitcnt vmcnt(2)
	ds_write2_b32 v25, v48, v49 offset1:1
	ds_write2_b32 v26, v50, v51 offset1:1
	ds_write2_b64 v19, v[36:37], v[38:39] offset1:1
	ds_write2_b32 v20, v40, v41 offset1:1
	ds_write2_b32 v21, v42, v43 offset1:1
	s_waitcnt vmcnt(1)
	ds_write_b128 v16, v[52:55] offset:4112
	s_waitcnt vmcnt(0)
	ds_write2_b32 v22, v56, v57 offset1:1
	ds_write2_b32 v23, v58, v59 offset1:1
	s_waitcnt lgkmcnt(0)
	s_barrier
	ds_read_b32 v28, v27 offset:1028
	ds_read_b32 v29, v27 offset:3084
	ds_read_b32 v30, v27 offset:5140
	ds_read_b32 v31, v27 offset:7196
	ds_read_b32 v32, v27 offset:6168
	ds_read_b32 v33, v27 offset:4112
	ds_read_b32 v34, v27 offset:2056
	ds_read_b32 v35, v27
	s_waitcnt lgkmcnt(0)
	v_cvt_pk_bf16_f32 v28, v35, v28
	v_cvt_pk_bf16_f32 v29, v34, v29
	v_cvt_pk_bf16_f32 v30, v33, v30
	v_cvt_pk_bf16_f32 v31, v32, v31
	ds_read_b32 v36, v27 offset:1060
	ds_read_b32 v37, v27 offset:3116
	ds_read_b32 v38, v27 offset:5172
	ds_read_b32 v39, v27 offset:7228
	ds_read_b32 v40, v27 offset:6200
	ds_read_b32 v41, v27 offset:4144
	ds_read_b32 v42, v27 offset:2088
	ds_read_b32 v43, v27 offset:32
	v_lshl_add_u64 v[32:33], s[6:7], 0, v[2:3]
	v_lshl_add_u64 v[34:35], v[32:33], 0, v[10:11]
	global_store_dwordx4 v[34:35], v[28:31], off
	v_lshl_add_u64 v[34:35], v[4:5], 1, v[32:33]
	s_cselect_b64 s[6:7], -1, 0
	s_waitcnt lgkmcnt(0)
	v_cvt_pk_bf16_f32 v28, v43, v36
	v_cvt_pk_bf16_f32 v29, v42, v37
	v_cvt_pk_bf16_f32 v30, v41, v38
	v_cvt_pk_bf16_f32 v31, v40, v39
	ds_read_b32 v11, v27 offset:1092
	ds_read_b32 v36, v27 offset:3148
	ds_read_b32 v37, v27 offset:6232
	ds_read_b32 v38, v27 offset:4176
	ds_read_b32 v39, v27 offset:2120
	ds_read_b32 v40, v27 offset:64
	ds_read_b32 v41, v27 offset:5204
	ds_read_b32 v42, v27 offset:7260
	global_store_dwordx4 v[34:35], v[28:31], off
	v_lshl_add_u64 v[34:35], v[6:7], 1, v[32:33]
	v_lshl_add_u64 v[32:33], v[8:9], 1, v[32:33]
	s_waitcnt lgkmcnt(2)
	v_cvt_pk_bf16_f32 v28, v40, v11
	v_cvt_pk_bf16_f32 v29, v39, v36
	s_waitcnt lgkmcnt(1)
	v_cvt_pk_bf16_f32 v30, v38, v41
	s_waitcnt lgkmcnt(0)
	v_cvt_pk_bf16_f32 v31, v37, v42
	ds_read_b32 v11, v27 offset:1124
	ds_read_b32 v36, v27 offset:3180
	ds_read_b32 v37, v27 offset:6264
	ds_read_b32 v38, v27 offset:4208
	ds_read_b32 v39, v27 offset:2152
	ds_read_b32 v40, v27 offset:96
	ds_read_b32 v41, v27 offset:5236
	ds_read_b32 v42, v27 offset:7292
	global_store_dwordx4 v[34:35], v[28:31], off
	s_waitcnt lgkmcnt(2)
	s_nop 0
	v_cvt_pk_bf16_f32 v28, v40, v11
	v_cvt_pk_bf16_f32 v29, v39, v36
	s_waitcnt lgkmcnt(1)
	v_cvt_pk_bf16_f32 v30, v38, v41
	s_waitcnt lgkmcnt(0)
	v_cvt_pk_bf16_f32 v31, v37, v42
	global_store_dwordx4 v[32:33], v[28:31], off
	s_branch .LBB0_1288

; #define LAS __attribute__((address_space(3)))
; #define SEAM(k) do { if (IN(k) && IN((k) + 1)) xcd_barrier(bar); \
;         if (PROBE_MASK) { const unsigned long long t_ = __builtin_amdgcn_s_memrealtime(); if ((PROBE_MASK >> (k)) & 1u) pr_acc += t_ - pr_t0; pr_t0 = t_; } } while (0)
; __device__ __forceinline__ void convert_deferred(const Ptrs& P, unsigned char* lds, int quota) {
;     const int tid = threadIdx.x, wid = tid >> 6, lane = tid & 63;
;     float* tile = (float*)lds;
;     volatile __attribute__((address_space(3))) int* slot = (volatile __attribute__((address_space(3))) int*)((__attribute__((address_space(3))) unsigned char*)lds + 131072 + 320 + 11000);
;     unsigned* q = (unsigned*)(P.ws + WS_CTL) + CW_DEFQ;
;     for (int n = 0; n < quota; ++n) {
;         __syncthreads();
;         if (tid == 0) *slot = (int)atomicAdd(q, 1u);
;         __syncthreads();
;         const int t = *slot;
;         if (t >= DEF_GU + DEF_DN) break;
;         const bool gu = t < DEF_GU;
;         const float* src = gu ? P.in[34] : P.in[36]; bf16* dst = (bf16*)(P.ws + (gu ? WS_WGU : WS_WDN));
;         const int N = gu ? 2048 : 1024, ntn = N / 256, it = gu ? 2 * NE * 16 * 8 - DEF_GU + t : 2 * NE * 16 * 4 - DEF_DN + (t - DEF_GU);
; __global__ void __launch_bounds__(NT, 2) mega(Args args) {
;     ...
;     if (IN(9)) { g8::MoeOrder S{(const char*)(ws + WS_ACT), (const char*)(ws + WS_WDN) + (size_t)0 * NE * 1024 * 1024 * 2, nullptr, (size_t)1024 * 1024 * 2, 4, D, G, vcu, 0, nullptr};
;         S.init((const unsigned*)(ws + WS_CTL) + CW_CNT + 0 * 64, (LAS int*)(LDSP + MISC_OFF + 256)); g8::EpiMoe2 E{P, 0}; g8::gemm_phase<g8::EpiMoe2, g8::MoeOrder, false, true>(LDSP, D, D, S, E);
;         { const int rem_ = ((LAS int*)(LDSP + MISC_OFF + 256))[96] % G; if (rem_ != 0 && vcu >= rem_) convert_deferred(P, lds, 5); } } SEAM(9);
.LBB0_1609:
	s_abs_i32 s0, s62
	v_cvt_f32_u32_e32 v2, s0
	s_sub_i32 s5, 0, s0
	s_abs_i32 s4, s9
	s_ashr_i32 s3, s9, 31
	v_rcp_iflag_f32_e32 v2, v2
	s_mov_b32 s1, 0
	v_mul_f32_e32 v2, 0x4f7ffffe, v2
	v_cvt_u32_f32_e32 v2, v2
	s_nop 0
	v_readfirstlane_b32 s6, v2
	s_mul_i32 s5, s5, s6
	s_mul_hi_u32 s5, s6, s5
	s_add_i32 s6, s6, s5
	s_mul_hi_u32 s5, s4, s6
	s_mul_i32 s5, s5, s0
	s_sub_i32 s4, s4, s5
	s_sub_i32 s5, s4, s0
	s_cmp_ge_u32 s4, s0
	s_cselect_b32 s4, s5, s4
	s_sub_i32 s5, s4, s0
	s_cmp_ge_u32 s4, s0
	s_cselect_b32 s0, s5, s4
	s_xor_b32 s0, s0, s3
	s_sub_i32 s0, s0, s3
	s_cmp_eq_u32 s0, 0
	v_readlane_b32 s3, v254, 2
	s_cselect_b64 s[4:5], -1, 0
	s_cmp_lt_i32 s3, s0
	s_cselect_b64 s[6:7], -1, 0
	s_or_b64 s[4:5], s[4:5], s[6:7]
	s_and_b64 vcc, exec, s[4:5]
	s_cbranch_vccnz .LBB0_1619
	v_and_b32_e32 v2, 0x7c, v175
	v_lshlrev_b32_e32 v3, 5, v0
	s_movk_i32 s0, 0x400
	v_and_or_b32 v12, v3, s0, v2
	v_bfe_u32 v2, v0, 3, 3
	v_lshl_or_b32 v4, v1, 5, v2
	v_lshlrev_b32_e32 v2, 3, v0
	v_lshl_add_u32 v11, v182, 4, 0
	v_and_b32_e32 v2, 56, v2
	v_mul_u32_u24_e32 v16, 0x2020, v1
	v_mov_b32_e32 v3, 0
	v_lshl_add_u32 v27, v4, 2, 0
	v_mul_u32_u24_e32 v28, 0x404, v2
	v_lshlrev_b32_e32 v10, 6, v4
	s_add_i32 s10, 0, 0x22c38
	v_add_u32_e32 v16, v11, v16
	s_mov_b32 s3, 7
	v_and_b32_e32 v13, 0xfc, v175
	v_and_b32_e32 v14, 56, v173
	v_or_b32_e32 v4, 0x200, v10
	v_mov_b32_e32 v5, v3
	v_or_b32_e32 v6, 0x400, v10
	v_mov_b32_e32 v7, v3
	v_or_b32_e32 v8, 0x600, v10
	v_mov_b32_e32 v9, v3
	v_mov_b32_e32 v15, s10
	s_movk_i32 s11, 0x1193
	s_movk_i32 s12, 0x800
	s_mov_b32 s13, 0x1104e000
	s_movk_i32 s14, -404
	v_add_u32_e32 v17, 0x404, v16
	v_add_u32_e32 v18, 0x40c, v16
	v_add_u32_e32 v19, 0x808, v16
	v_add_u32_e32 v20, 0xc0c, v16
	v_add_u32_e32 v21, 0xc14, v16
	v_add_u32_e32 v22, 0x1414, v16
	v_add_u32_e32 v23, 0x141c, v16
	v_add_u32_e32 v24, 0x1818, v16
	v_add_u32_e32 v25, 0x1c1c, v16
	v_add_u32_e32 v26, 0x1c24, v16
	v_lshlrev_b32_e32 v2, 1, v2
	v_add_u32_e32 v27, v27, v28
	v_lshlrev_b32_e32 v10, 1, v10
	s_branch .LBB0_1612

; __device__ __forceinline__ unsigned g8_cvt_pk(float lo, float hi) { unsigned r; asm volatile("v_cvt_pk_bf16_f32 %0, %1, %2" : "=v"(r) : "v"(lo), "v"(hi)); return r; }
; __device__ __forceinline__ void convert_deferred(const Ptrs& P, unsigned char* lds, int quota) {
;     ...
;         const int t = *slot;
;         if (t >= DEF_GU + DEF_DN) break;
;         const bool gu = t < DEF_GU;
;         const float* src = gu ? P.in[34] : P.in[36]; bf16* dst = (bf16*)(P.ws + (gu ? WS_WGU : WS_WDN));
;         const int N = gu ? 2048 : 1024, ntn = N / 256, it = gu ? 2 * NE * 16 * 8 - DEF_GU + t : 2 * NE * 16 * 4 - DEF_DN + (t - DEF_GU);
;         f32x4 cur[8];
;         bt_load(src, N, gu ? 1 : 0, it, ntn, cur);
; #pragma unroll
;         for (int i = 0; i < 8; ++i) { float* tp = tile + (wid * 8 + i) * 257 + lane * 4; tp[0] = cur[i][0]; tp[1] = cur[i][1]; tp[2] = cur[i][2]; tp[3] = cur[i][3]; }
;         __syncthreads();
;         const int per = 16 * ntn, z = it / per, r = it % per, kt = r / ntn, nt = r % ntn;
;         bf16* d = dst + (size_t)z * N * 1024 + (((size_t)nt * 16 + kt) << 14);
;         const int kc = lane & 7;
; #pragma unroll
;         for (int pss = 0; pss < 4; ++pss) {
;             const int nn = wid * 32 + pss * 8 + (lane >> 3); float f[8];
; #pragma unroll
;             for (int j = 0; j < 8; ++j) f[j] = tile[(kc * 8 + j) * 257 + nn];
;             u32x4 w; w.x = g8_cvt_pk(f[0], f[1]); w.y = g8_cvt_pk(f[2], f[3]); w.z = g8_cvt_pk(f[4], f[5]); w.w = g8_cvt_pk(f[6], f[7]);
;             *(u32x4*)(d + nn * 64 + kc * 8) = w;
;         }
.LBB0_1616:
	s_or_b64 exec, exec, s[4:5]
	s_waitcnt lgkmcnt(0)
	s_barrier
	ds_read_b32 v11, v15
	s_mov_b64 s[4:5], -1
	s_waitcnt lgkmcnt(0)
	v_cmp_lt_i32_e32 vcc, s11, v11
	v_readfirstlane_b32 s0, v11
	s_cbranch_vccnz .LBB0_1611
	s_cmpk_gt_i32 s0, 0xbb7
	s_cselect_b64 vcc, -1, 0
	s_and_b64 s[4:5], vcc, exec
	s_cselect_b32 s4, s13, 0x104e000
	s_cselect_b32 s9, 0x400, s12
	s_cselect_b32 s15, s73, s69
	s_cselect_b32 s18, s72, s68
	s_cselect_b32 s5, s14, 0x1448
	s_cselect_b32 s16, 20, 21
	s_cselect_b32 s19, 10, 11
	s_add_u32 s20, s78, s4
	s_addc_u32 s21, s79, 0
	s_lshr_b32 s6, s9, 4
	s_abs_i32 s4, s6
	v_cvt_f32_u32_e32 v11, s4
	s_sub_i32 s17, 0, s4
	s_add_i32 s5, s5, s0
	s_abs_i32 s7, s5
	v_rcp_iflag_f32_e32 v11, v11
	s_xor_b32 s0, s5, s6
	s_lshr_b32 s8, s9, 8
	s_ashr_i32 s0, s0, 31
	v_mul_f32_e32 v11, 0x4f7ffffe, v11
	v_cvt_u32_f32_e32 v11, v11
	s_nop 0
	v_readfirstlane_b32 s22, v11
	s_mul_i32 s17, s17, s22
	s_mul_hi_u32 s17, s22, s17
	s_add_i32 s22, s22, s17
	s_mul_hi_u32 s17, s7, s22
	s_mul_i32 s22, s17, s4
	s_sub_i32 s7, s7, s22
	s_add_i32 s22, s17, 1
	s_sub_i32 s23, s7, s4
	s_cmp_ge_u32 s7, s4
	s_cselect_b32 s17, s22, s17
	s_cselect_b32 s7, s23, s7
	s_add_i32 s22, s17, 1
	s_cmp_ge_u32 s7, s4
	s_cselect_b32 s4, s22, s17
	s_xor_b32 s4, s4, s0
	s_sub_i32 s4, s4, s0
	s_sext_i32_i8 s0, s8
	v_cvt_f32_i32_e32 v11, s0
	s_mul_i32 s6, s4, s6
	s_sub_i32 s5, s5, s6
	v_cvt_f32_i32_e32 v28, s5
	v_rcp_iflag_f32_e32 v29, v11
	s_xor_b32 s0, s5, s0
	s_ashr_i32 s0, s0, 30
	s_or_b32 s0, s0, 1
	v_mul_f32_e32 v29, v28, v29
	v_trunc_f32_e32 v29, v29
	v_fma_f32 v28, -v29, v11, v28
	v_cvt_i32_f32_e32 v29, v29
	v_cmp_ge_f32_e64 s[6:7], |v28|, |v11|
	s_and_b64 s[6:7], s[6:7], exec
	s_cselect_b32 s0, s0, 0
	v_readfirstlane_b32 s6, v29
	s_add_i32 s6, s6, s0
	s_mul_i32 s7, s6, s8
	s_sub_i32 s8, s5, s7
	s_sext_i32_i8 s5, s8
	v_lshl_add_u32 v11, s5, 7, v12
	v_lshl_or_b32 v28, s5, 8, v13
	s_ashr_i32 s5, s4, 31
	s_sext_i32_i8 s0, s6
	s_lshl_b64 s[16:17], s[4:5], s16
	v_lshl_or_b32 v30, s0, 6, v14
	s_lshl_b64 s[16:17], s[16:17], 2
	v_ashrrev_i32_e32 v31, 31, v30
	s_add_u32 s16, s18, s16
	v_cndmask_b32_e32 v28, v11, v28, vcc
	s_addc_u32 s17, s15, s17
	v_lshlrev_b64 v[30:31], s19, v[30:31]
	v_lshl_add_u64 v[30:31], v[30:31], 2, s[16:17]
	v_ashrrev_i32_e32 v29, 31, v28
	v_lshl_add_u64 v[52:53], v[28:29], 2, v[30:31]
	s_lshl_b64 s[16:17], 12, s19
	s_lshl_b32 s0, s9, 2
	v_lshl_add_u64 v[40:41], v[52:53], 0, s[16:17]
	s_lshl_b64 s[16:17], 24, s19
	v_lshl_add_u64 v[36:37], v[52:53], 0, s[0:1]
	v_lshl_add_u64 v[44:45], v[52:53], 0, s[16:17]
	s_lshl_b64 s[16:17], 28, s19
	v_lshl_add_u64 v[54:55], v[36:37], 0, s[0:1]
	v_lshl_add_u64 v[48:49], v[52:53], 0, s[16:17]
	s_lshl_b32 s0, s9, 3
	s_lshl_b64 s[16:17], 20, s19
	global_load_dwordx4 v[28:31], v[52:53], off nt
	global_load_dwordx4 v[32:35], v[36:37], off nt
	s_nop 0
	global_load_dwordx4 v[36:39], v[54:55], off nt
	s_nop 0
	global_load_dwordx4 v[40:43], v[40:41], off nt
	v_lshl_add_u64 v[54:55], v[54:55], 0, s[0:1]
	v_lshl_add_u64 v[56:57], v[52:53], 0, s[16:17]
	global_load_dwordx4 v[44:47], v[44:45], off nt
	s_nop 0
	global_load_dwordx4 v[48:51], v[48:49], off nt
	s_nop 0
	global_load_dwordx4 v[52:55], v[54:55], off nt
	s_nop 0
	global_load_dwordx4 v[56:59], v[56:57], off nt
	s_lshl_b64 s[4:5], s[4:5], s19
	s_lshl_b64 s[4:5], s[4:5], 11
	s_add_u32 s0, s20, s4
	s_addc_u32 s9, s21, s5
	s_bfe_i64 s[4:5], s[8:9], 0x80000
	s_bfe_i64 s[6:7], s[6:7], 0x80000
	s_lshl_b64 s[4:5], s[4:5], 19
	s_add_u32 s0, s0, s4
	s_addc_u32 s8, s9, s5
	s_lshl_b64 s[4:5], s[6:7], 15
	s_add_u32 s4, s0, s4
	s_addc_u32 s5, s8, s5
	v_mov_b32_e32 v11, v3
	s_add_i32 s3, s3, -1
	s_cmp_eq_u32 s3, 0
	s_waitcnt vmcnt(7)
	ds_write_b128 v16, v[28:31]
	s_waitcnt vmcnt(6)
	ds_write2_b32 v17, v32, v33 offset1:1
	ds_write2_b32 v18, v34, v35 offset1:1
	s_waitcnt vmcnt(3)
	ds_write2_b64 v24, v[44:45], v[46:47] offset1:1
	s_waitcnt vmcnt(2)
	ds_write2_b32 v25, v48, v49 offset1:1
	ds_write2_b32 v26, v50, v51 offset1:1
	ds_write2_b64 v19, v[36:37], v[38:39] offset1:1
	ds_write2_b32 v20, v40, v41 offset1:1
	ds_write2_b32 v21, v42, v43 offset1:1
	s_waitcnt vmcnt(1)
	ds_write_b128 v16, v[52:55] offset:4112
	s_waitcnt vmcnt(0)
	ds_write2_b32 v22, v56, v57 offset1:1
	ds_write2_b32 v23, v58, v59 offset1:1
	s_waitcnt lgkmcnt(0)
	s_barrier
	ds_read_b32 v28, v27 offset:1028
	ds_read_b32 v29, v27 offset:3084
	ds_read_b32 v30, v27 offset:5140
	ds_read_b32 v31, v27 offset:7196
	ds_read_b32 v32, v27 offset:6168
	ds_read_b32 v33, v27 offset:4112
	ds_read_b32 v34, v27 offset:2056
	ds_read_b32 v35, v27
	s_waitcnt lgkmcnt(0)
	v_cvt_pk_bf16_f32 v28, v35, v28
	v_cvt_pk_bf16_f32 v29, v34, v29
	v_cvt_pk_bf16_f32 v30, v33, v30
	v_cvt_pk_bf16_f32 v31, v32, v31
	ds_read_b32 v36, v27 offset:1060
	ds_read_b32 v37, v27 offset:3116
	ds_read_b32 v38, v27 offset:5172
	ds_read_b32 v39, v27 offset:7228
	ds_read_b32 v40, v27 offset:6200
	ds_read_b32 v41, v27 offset:4144
	ds_read_b32 v42, v27 offset:2088
	ds_read_b32 v43, v27 offset:32
	v_lshl_add_u64 v[32:33], s[4:5], 0, v[2:3]
	v_lshl_add_u64 v[34:35], v[32:33], 0, v[10:11]
	global_store_dwordx4 v[34:35], v[28:31], off
	v_lshl_add_u64 v[34:35], v[4:5], 1, v[32:33]
	s_cselect_b64 s[4:5], -1, 0
	s_waitcnt lgkmcnt(0)
	v_cvt_pk_bf16_f32 v28, v43, v36
	v_cvt_pk_bf16_f32 v29, v42, v37
	v_cvt_pk_bf16_f32 v30, v41, v38
	v_cvt_pk_bf16_f32 v31, v40, v39
	ds_read_b32 v11, v27 offset:1092
	ds_read_b32 v36, v27 offset:3148
	ds_read_b32 v37, v27 offset:6232
	ds_read_b32 v38, v27 offset:4176
	ds_read_b32 v39, v27 offset:2120
	ds_read_b32 v40, v27 offset:64
	ds_read_b32 v41, v27 offset:5204
	ds_read_b32 v42, v27 offset:7260
	global_store_dwordx4 v[34:35], v[28:31], off
	v_lshl_add_u64 v[34:35], v[6:7], 1, v[32:33]
	v_lshl_add_u64 v[32:33], v[8:9], 1, v[32:33]
	s_waitcnt lgkmcnt(2)
	v_cvt_pk_bf16_f32 v28, v40, v11
	v_cvt_pk_bf16_f32 v29, v39, v36
	s_waitcnt lgkmcnt(1)
	v_cvt_pk_bf16_f32 v30, v38, v41
	s_waitcnt lgkmcnt(0)
	v_cvt_pk_bf16_f32 v31, v37, v42
	ds_read_b32 v11, v27 offset:1124
	ds_read_b32 v36, v27 offset:3180
	ds_read_b32 v37, v27 offset:6264
	ds_read_b32 v38, v27 offset:4208
	ds_read_b32 v39, v27 offset:2152
	ds_read_b32 v40, v27 offset:96
	ds_read_b32 v41, v27 offset:5236
	ds_read_b32 v42, v27 offset:7292
	global_store_dwordx4 v[34:35], v[28:31], off
	s_waitcnt lgkmcnt(2)
	s_nop 0
	v_cvt_pk_bf16_f32 v28, v40, v11
	v_cvt_pk_bf16_f32 v29, v39, v36
	s_waitcnt lgkmcnt(1)
	v_cvt_pk_bf16_f32 v30, v38, v41
	s_waitcnt lgkmcnt(0)
	v_cvt_pk_bf16_f32 v31, v37, v42
	global_store_dwordx4 v[32:33], v[28:31], off
	s_branch .LBB0_1611

; #define LAS __attribute__((address_space(3)))
; #define SEAM(k) do { if (IN(k) && IN((k) + 1)) xcd_barrier(bar); \
;         if (PROBE_MASK) { const unsigned long long t_ = __builtin_amdgcn_s_memrealtime(); if ((PROBE_MASK >> (k)) & 1u) pr_acc += t_ - pr_t0; pr_t0 = t_; } } while (0)
; __device__ __forceinline__ void convert_deferred(const Ptrs& P, unsigned char* lds, int quota) {
;     const int tid = threadIdx.x, wid = tid >> 6, lane = tid & 63;
;     float* tile = (float*)lds;
;     volatile __attribute__((address_space(3))) int* slot = (volatile __attribute__((address_space(3))) int*)((__attribute__((address_space(3))) unsigned char*)lds + 131072 + 320 + 11000);
;     unsigned* q = (unsigned*)(P.ws + WS_CTL) + CW_DEFQ;
;     for (int n = 0; n < quota; ++n) {
;         __syncthreads();
;         if (tid == 0) *slot = (int)atomicAdd(q, 1u);
;         __syncthreads();
;         const int t = *slot;
;         if (t >= DEF_GU + DEF_DN) break;
;         const bool gu = t < DEF_GU;
;         const float* src = gu ? P.in[34] : P.in[36]; bf16* dst = (bf16*)(P.ws + (gu ? WS_WGU : WS_WDN));
;         const int N = gu ? 2048 : 1024, ntn = N / 256, it = gu ? 2 * NE * 16 * 8 - DEF_GU + t : 2 * NE * 16 * 4 - DEF_DN + (t - DEF_GU);
; __global__ void __launch_bounds__(NT, 2) mega(Args args) {
;     ...
;     if (IN(11)) { g8::DenseOrder S; S.init(H, D, (const bf16*)(ws + WS_WODIN), D, R, ODD_IN, G, (int)blockIdx.x, 0);
;         g8::EpiDiffIn E{Z, P.in[25], P.in[26], (const float*)(ws + WS_ROPE), (const float*)(ws + WS_ROPE) + SEQ * 64, (LAS float*)(LDSP + MISC_OFF + 1024)};
;         g8::gemm_phase<g8::EpiDiffIn, g8::DenseOrder, false, true>(LDSP, D, D, S, E);
;         if (IDLE_LAST(68 * 12)) convert_deferred(P, lds, 4); } SEAM(11);
.LBB0_1851:
	s_abs_i32 s0, s62
	v_cvt_f32_u32_e32 v2, s0
	s_sub_i32 s3, 0, s0
	v_readlane_b32 s56, v254, 40
	s_mov_b32 s1, 0
	v_rcp_iflag_f32_e32 v2, v2
	v_readlane_b32 s57, v254, 41
	v_mul_f32_e32 v2, 0x4f7ffffe, v2
	v_cvt_u32_f32_e32 v2, v2
	s_nop 0
	v_readfirstlane_b32 s4, v2
	s_mul_i32 s3, s3, s4
	s_mul_hi_u32 s3, s4, s3
	s_add_i32 s4, s4, s3
	s_mul_hi_u32 s3, s4, 0x330
	s_mul_i32 s3, s3, s0
	s_sub_i32 s3, 0x330, s3
	s_sub_i32 s4, s3, s0
	s_cmp_ge_u32 s3, s0
	s_cselect_b32 s3, s4, s3
	s_sub_i32 s4, s3, s0
	s_cmp_ge_u32 s3, s0
	s_cselect_b32 s0, s4, s3
	s_cmp_eq_u32 s0, 0
	s_cselect_b64 s[4:5], -1, 0
	s_cmp_lt_i32 s2, s0
	s_cselect_b64 s[6:7], -1, 0
	s_or_b64 s[4:5], s[4:5], s[6:7]
	s_and_b64 vcc, exec, s[4:5]
	s_cbranch_vccnz .LBB0_1861
	v_and_b32_e32 v2, 0x7c, v218
	v_lshlrev_b32_e32 v3, 5, v0
	s_movk_i32 s0, 0x400
	v_and_or_b32 v12, v3, s0, v2
	v_bfe_u32 v2, v0, 3, 3
	v_lshl_or_b32 v4, v1, 5, v2
	v_lshlrev_b32_e32 v2, 3, v0
	v_lshl_add_u32 v11, v182, 4, 0
	v_and_b32_e32 v2, 56, v2
	v_mul_u32_u24_e32 v16, 0x2020, v1
	v_mov_b32_e32 v3, 0
	s_waitcnt vmcnt(0)
	v_lshl_add_u32 v27, v4, 2, 0
	v_mul_u32_u24_e32 v28, 0x404, v2
	v_lshlrev_b32_e32 v10, 6, v4
	s_add_i32 s10, 0, 0x22c38
	v_add_u32_e32 v16, v11, v16
	v_and_b32_e32 v13, 0xfc, v218
	v_and_b32_e32 v14, 56, v179
	s_mov_b32 s3, 8
	v_or_b32_e32 v4, 0x200, v10
	v_mov_b32_e32 v5, v3
	v_or_b32_e32 v6, 0x400, v10
	v_mov_b32_e32 v7, v3
	v_or_b32_e32 v8, 0x600, v10
	v_mov_b32_e32 v9, v3
	v_mov_b32_e32 v15, s10
	s_movk_i32 s11, 0x1193
	s_movk_i32 s12, 0x800
	s_mov_b32 s13, 0x1104e000
	s_movk_i32 s14, -404
	v_add_u32_e32 v17, 0x404, v16
	v_add_u32_e32 v18, 0x40c, v16
	v_add_u32_e32 v19, 0x808, v16
	v_add_u32_e32 v20, 0xc0c, v16
	v_add_u32_e32 v21, 0xc14, v16
	v_add_u32_e32 v22, 0x1414, v16
	v_add_u32_e32 v23, 0x141c, v16
	v_add_u32_e32 v24, 0x1818, v16
	v_add_u32_e32 v25, 0x1c1c, v16
	v_add_u32_e32 v26, 0x1c24, v16
	v_lshlrev_b32_e32 v2, 1, v2
	v_add_u32_e32 v27, v27, v28
	v_lshlrev_b32_e32 v10, 1, v10
	s_branch .LBB0_1854

; __device__ __forceinline__ unsigned g8_cvt_pk(float lo, float hi) { unsigned r; asm volatile("v_cvt_pk_bf16_f32 %0, %1, %2" : "=v"(r) : "v"(lo), "v"(hi)); return r; }
; __device__ __forceinline__ void convert_deferred(const Ptrs& P, unsigned char* lds, int quota) {
;     ...
;         const int t = *slot;
;         if (t >= DEF_GU + DEF_DN) break;
;         const bool gu = t < DEF_GU;
;         const float* src = gu ? P.in[34] : P.in[36]; bf16* dst = (bf16*)(P.ws + (gu ? WS_WGU : WS_WDN));
;         const int N = gu ? 2048 : 1024, ntn = N / 256, it = gu ? 2 * NE * 16 * 8 - DEF_GU + t : 2 * NE * 16 * 4 - DEF_DN + (t - DEF_GU);
;         f32x4 cur[8];
;         bt_load(src, N, gu ? 1 : 0, it, ntn, cur);
; #pragma unroll
;         for (int i = 0; i < 8; ++i) { float* tp = tile + (wid * 8 + i) * 257 + lane * 4; tp[0] = cur[i][0]; tp[1] = cur[i][1]; tp[2] = cur[i][2]; tp[3] = cur[i][3]; }
;         __syncthreads();
;         const int per = 16 * ntn, z = it / per, r = it % per, kt = r / ntn, nt = r % ntn;
;         bf16* d = dst + (size_t)z * N * 1024 + (((size_t)nt * 16 + kt) << 14);
;         const int kc = lane & 7;
; #pragma unroll
;         for (int pss = 0; pss < 4; ++pss) {
;             const int nn = wid * 32 + pss * 8 + (lane >> 3); float f[8];
; #pragma unroll
;             for (int j = 0; j < 8; ++j) f[j] = tile[(kc * 8 + j) * 257 + nn];
;             u32x4 w; w.x = g8_cvt_pk(f[0], f[1]); w.y = g8_cvt_pk(f[2], f[3]); w.z = g8_cvt_pk(f[4], f[5]); w.w = g8_cvt_pk(f[6], f[7]);
;             *(u32x4*)(d + nn * 64 + kc * 8) = w;
;         }
.LBB0_1858:
	s_or_b64 exec, exec, s[4:5]
	s_waitcnt lgkmcnt(0)
	s_barrier
	ds_read_b32 v11, v15
	s_mov_b64 s[4:5], -1
	s_waitcnt lgkmcnt(0)
	v_cmp_lt_i32_e32 vcc, s11, v11
	v_readfirstlane_b32 s0, v11
	s_cbranch_vccnz .LBB0_1853
	s_cmpk_gt_i32 s0, 0xbb7
	s_cselect_b64 vcc, -1, 0
	s_and_b64 s[4:5], vcc, exec
	s_cselect_b32 s4, s13, 0x104e000
	s_cselect_b32 s9, 0x400, s12
	s_cselect_b32 s15, s73, s69
	s_cselect_b32 s20, s72, s68
	s_cselect_b32 s5, s14, 0x1448
	s_cselect_b32 s16, 20, 21
	s_cselect_b32 s21, 10, 11
	s_add_u32 s22, s78, s4
	s_addc_u32 s23, s79, 0
	s_lshr_b32 s6, s9, 4
	s_abs_i32 s4, s6
	v_cvt_f32_u32_e32 v11, s4
	s_sub_i32 s17, 0, s4
	s_add_i32 s5, s5, s0
	s_abs_i32 s7, s5
	v_rcp_iflag_f32_e32 v11, v11
	s_xor_b32 s0, s5, s6
	s_lshr_b32 s8, s9, 8
	s_ashr_i32 s0, s0, 31
	v_mul_f32_e32 v11, 0x4f7ffffe, v11
	v_cvt_u32_f32_e32 v11, v11
	s_nop 0
	v_readfirstlane_b32 s24, v11
	s_mul_i32 s17, s17, s24
	s_mul_hi_u32 s17, s24, s17
	s_add_i32 s24, s24, s17
	s_mul_hi_u32 s17, s7, s24
	s_mul_i32 s24, s17, s4
	s_sub_i32 s7, s7, s24
	s_add_i32 s24, s17, 1
	s_sub_i32 s25, s7, s4
	s_cmp_ge_u32 s7, s4
	s_cselect_b32 s17, s24, s17
	s_cselect_b32 s7, s25, s7
	s_add_i32 s24, s17, 1
	s_cmp_ge_u32 s7, s4
	s_cselect_b32 s4, s24, s17
	s_xor_b32 s4, s4, s0
	s_sub_i32 s4, s4, s0
	s_sext_i32_i8 s0, s8
	v_cvt_f32_i32_e32 v11, s0
	s_mul_i32 s6, s4, s6
	s_sub_i32 s5, s5, s6
	v_cvt_f32_i32_e32 v28, s5
	v_rcp_iflag_f32_e32 v29, v11
	s_xor_b32 s0, s5, s0
	s_ashr_i32 s0, s0, 30
	s_or_b32 s0, s0, 1
	v_mul_f32_e32 v29, v28, v29
	v_trunc_f32_e32 v29, v29
	v_fma_f32 v28, -v29, v11, v28
	v_cvt_i32_f32_e32 v29, v29
	v_cmp_ge_f32_e64 s[6:7], |v28|, |v11|
	s_and_b64 s[6:7], s[6:7], exec
	s_cselect_b32 s0, s0, 0
	v_readfirstlane_b32 s6, v29
	s_add_i32 s6, s6, s0
	s_mul_i32 s7, s6, s8
	s_sub_i32 s8, s5, s7
	s_sext_i32_i8 s5, s8
	v_lshl_add_u32 v11, s5, 7, v12
	v_lshl_or_b32 v28, s5, 8, v13
	s_ashr_i32 s5, s4, 31
	s_sext_i32_i8 s0, s6
	s_lshl_b64 s[16:17], s[4:5], s16
	v_lshl_or_b32 v30, s0, 6, v14
	s_lshl_b64 s[16:17], s[16:17], 2
	v_ashrrev_i32_e32 v31, 31, v30
	s_add_u32 s16, s20, s16
	v_cndmask_b32_e32 v28, v11, v28, vcc
	s_addc_u32 s17, s15, s17
	v_lshlrev_b64 v[30:31], s21, v[30:31]
	v_lshl_add_u64 v[30:31], v[30:31], 2, s[16:17]
	v_ashrrev_i32_e32 v29, 31, v28
	v_lshl_add_u64 v[52:53], v[28:29], 2, v[30:31]
	s_lshl_b64 s[16:17], 12, s21
	s_lshl_b32 s0, s9, 2
	v_lshl_add_u64 v[40:41], v[52:53], 0, s[16:17]
	s_lshl_b64 s[16:17], 24, s21
	v_lshl_add_u64 v[36:37], v[52:53], 0, s[0:1]
	v_lshl_add_u64 v[44:45], v[52:53], 0, s[16:17]
	s_lshl_b64 s[16:17], 28, s21
	v_lshl_add_u64 v[54:55], v[36:37], 0, s[0:1]
	v_lshl_add_u64 v[48:49], v[52:53], 0, s[16:17]
	s_lshl_b32 s0, s9, 3
	s_lshl_b64 s[16:17], 20, s21
	global_load_dwordx4 v[28:31], v[52:53], off nt
	global_load_dwordx4 v[32:35], v[36:37], off nt
	s_nop 0
	global_load_dwordx4 v[36:39], v[54:55], off nt
	s_nop 0
	global_load_dwordx4 v[40:43], v[40:41], off nt
	v_lshl_add_u64 v[54:55], v[54:55], 0, s[0:1]
	v_lshl_add_u64 v[56:57], v[52:53], 0, s[16:17]
	global_load_dwordx4 v[44:47], v[44:45], off nt
	s_nop 0
	global_load_dwordx4 v[48:51], v[48:49], off nt
	s_nop 0
	global_load_dwordx4 v[52:55], v[54:55], off nt
	s_nop 0
	global_load_dwordx4 v[56:59], v[56:57], off nt
	s_lshl_b64 s[4:5], s[4:5], s21
	s_lshl_b64 s[4:5], s[4:5], 11
	s_add_u32 s0, s22, s4
	s_addc_u32 s9, s23, s5
	s_bfe_i64 s[4:5], s[8:9], 0x80000
	s_bfe_i64 s[6:7], s[6:7], 0x80000
	s_lshl_b64 s[4:5], s[4:5], 19
	s_add_u32 s0, s0, s4
	s_addc_u32 s8, s9, s5
	s_lshl_b64 s[4:5], s[6:7], 15
	s_add_u32 s4, s0, s4
	s_addc_u32 s5, s8, s5
	v_mov_b32_e32 v11, v3
	s_add_i32 s3, s3, -1
	s_cmp_eq_u32 s3, 0
	s_waitcnt vmcnt(7)
	ds_write_b128 v16, v[28:31]
	s_waitcnt vmcnt(6)
	ds_write2_b32 v17, v32, v33 offset1:1
	ds_write2_b32 v18, v34, v35 offset1:1
	s_waitcnt vmcnt(3)
	ds_write2_b64 v24, v[44:45], v[46:47] offset1:1
	s_waitcnt vmcnt(2)
	ds_write2_b32 v25, v48, v49 offset1:1
	ds_write2_b32 v26, v50, v51 offset1:1
	ds_write2_b64 v19, v[36:37], v[38:39] offset1:1
	ds_write2_b32 v20, v40, v41 offset1:1
	ds_write2_b32 v21, v42, v43 offset1:1
	s_waitcnt vmcnt(1)
	ds_write_b128 v16, v[52:55] offset:4112
	s_waitcnt vmcnt(0)
	ds_write2_b32 v22, v56, v57 offset1:1
	ds_write2_b32 v23, v58, v59 offset1:1
	s_waitcnt lgkmcnt(0)
	s_barrier
	ds_read_b32 v28, v27 offset:1028
	ds_read_b32 v29, v27 offset:3084
	ds_read_b32 v30, v27 offset:5140
	ds_read_b32 v31, v27 offset:7196
	ds_read_b32 v32, v27 offset:6168
	ds_read_b32 v33, v27 offset:4112
	ds_read_b32 v34, v27 offset:2056
	ds_read_b32 v35, v27
	s_waitcnt lgkmcnt(0)
	v_cvt_pk_bf16_f32 v28, v35, v28
	v_cvt_pk_bf16_f32 v29, v34, v29
	v_cvt_pk_bf16_f32 v30, v33, v30
	v_cvt_pk_bf16_f32 v31, v32, v31
	ds_read_b32 v36, v27 offset:1060
	ds_read_b32 v37, v27 offset:3116
	ds_read_b32 v38, v27 offset:5172
	ds_read_b32 v39, v27 offset:7228
	ds_read_b32 v40, v27 offset:6200
	ds_read_b32 v41, v27 offset:4144
	ds_read_b32 v42, v27 offset:2088
	ds_read_b32 v43, v27 offset:32
	v_lshl_add_u64 v[32:33], s[4:5], 0, v[2:3]
	v_lshl_add_u64 v[34:35], v[32:33], 0, v[10:11]
	global_store_dwordx4 v[34:35], v[28:31], off
	v_lshl_add_u64 v[34:35], v[4:5], 1, v[32:33]
	s_cselect_b64 s[4:5], -1, 0
	s_waitcnt lgkmcnt(0)
	v_cvt_pk_bf16_f32 v28, v43, v36
	v_cvt_pk_bf16_f32 v29, v42, v37
	v_cvt_pk_bf16_f32 v30, v41, v38
	v_cvt_pk_bf16_f32 v31, v40, v39
	ds_read_b32 v11, v27 offset:1092
	ds_read_b32 v36, v27 offset:3148
	ds_read_b32 v37, v27 offset:6232
	ds_read_b32 v38, v27 offset:4176
	ds_read_b32 v39, v27 offset:2120
	ds_read_b32 v40, v27 offset:64
	ds_read_b32 v41, v27 offset:5204
	ds_read_b32 v42, v27 offset:7260
	global_store_dwordx4 v[34:35], v[28:31], off
	v_lshl_add_u64 v[34:35], v[6:7], 1, v[32:33]
	v_lshl_add_u64 v[32:33], v[8:9], 1, v[32:33]
	s_waitcnt lgkmcnt(2)
	v_cvt_pk_bf16_f32 v28, v40, v11
	v_cvt_pk_bf16_f32 v29, v39, v36
	s_waitcnt lgkmcnt(1)
	v_cvt_pk_bf16_f32 v30, v38, v41
	s_waitcnt lgkmcnt(0)
	v_cvt_pk_bf16_f32 v31, v37, v42
	ds_read_b32 v11, v27 offset:1124
	ds_read_b32 v36, v27 offset:3180
	ds_read_b32 v37, v27 offset:6264
	ds_read_b32 v38, v27 offset:4208
	ds_read_b32 v39, v27 offset:2152
	ds_read_b32 v40, v27 offset:96
	ds_read_b32 v41, v27 offset:5236
	ds_read_b32 v42, v27 offset:7292
	global_store_dwordx4 v[34:35], v[28:31], off
	s_waitcnt lgkmcnt(2)
	s_nop 0
	v_cvt_pk_bf16_f32 v28, v40, v11
	v_cvt_pk_bf16_f32 v29, v39, v36
	s_waitcnt lgkmcnt(1)
	v_cvt_pk_bf16_f32 v30, v38, v41
	s_waitcnt lgkmcnt(0)
	v_cvt_pk_bf16_f32 v31, v37, v42
	global_store_dwordx4 v[32:33], v[28:31], off
	s_branch .LBB0_1853

; #define SEAM(k) do { if (IN(k) && IN((k) + 1)) xcd_barrier(bar); \
;         if (PROBE_MASK) { const unsigned long long t_ = __builtin_amdgcn_s_memrealtime(); if ((PROBE_MASK >> (k)) & 1u) pr_acc += t_ - pr_t0; pr_t0 = t_; } } while (0)
; __device__ __forceinline__ void convert_deferred(const Ptrs& P, unsigned char* lds, int quota) {
;     const int tid = threadIdx.x, wid = tid >> 6, lane = tid & 63;
;     float* tile = (float*)lds;
;     volatile __attribute__((address_space(3))) int* slot = (volatile __attribute__((address_space(3))) int*)((__attribute__((address_space(3))) unsigned char*)lds + 131072 + 320 + 11000);
;     unsigned* q = (unsigned*)(P.ws + WS_CTL) + CW_DEFQ;
;     for (int n = 0; n < quota; ++n) {
;         __syncthreads();
;         if (tid == 0) *slot = (int)atomicAdd(q, 1u);
;         __syncthreads();
;         const int t = *slot;
;         if (t >= DEF_GU + DEF_DN) break;
;         const bool gu = t < DEF_GU;
;         const float* src = gu ? P.in[34] : P.in[36]; bf16* dst = (bf16*)(P.ws + (gu ? WS_WGU : WS_WDN));
;         const int N = gu ? 2048 : 1024, ntn = N / 256, it = gu ? 2 * NE * 16 * 8 - DEF_GU + t : 2 * NE * 16 * 4 - DEF_DN + (t - DEF_GU);
; __global__ void __launch_bounds__(NT, 2) mega(Args args) {
;     ...
;     if (IN(15)) { ph_norm2_router(P, lds, 1, 1); convert_deferred(P, lds, 1 << 20); } SEAM(15);
.LBB0_2278:
	v_and_b32_e32 v2, 0x7c, v179
	v_lshlrev_b32_e32 v3, 5, v0
	s_movk_i32 s0, 0x400
	v_and_or_b32 v12, v3, s0, v2
	v_lshrrev_b32_e32 v2, 3, v0
	v_and_b32_e32 v14, 56, v2
	v_lshrrev_b32_e32 v2, 3, v182
	v_lshl_or_b32 v4, v1, 5, v2
	v_lshl_add_u32 v5, v182, 4, 0
	v_and_b32_e32 v2, 56, v188
	v_lshl_add_u32 v7, v4, 2, 0
	v_mul_u32_u24_e32 v11, 0x2020, v1
	v_lshlrev_b32_e32 v4, 6, v4
	v_mul_u32_u24_e32 v9, 0x404, v2
	v_or_b32_e32 v6, 0x200, v4
	v_or_b32_e32 v8, 0x400, v4
	v_or_b32_e32 v10, 0x600, v4
	s_add_i32 s10, 0, 0x22c38
	v_add_u32_e32 v16, v5, v11
	v_and_b32_e32 v13, 0xfc, v179
	s_mov_b32 s1, 0
	v_mov_b32_e32 v3, 0
	s_mov_b32 s3, 0x100000
	v_mov_b32_e32 v15, s10
	s_movk_i32 s11, 0x1193
	s_movk_i32 s12, 0x800
	s_mov_b32 s13, 0x1104e000
	s_movk_i32 s14, -404
	v_add_u32_e32 v17, 0x404, v16
	v_add_u32_e32 v18, 0x40c, v16
	v_add_u32_e32 v19, 0x808, v16
	v_add_u32_e32 v20, 0xc0c, v16
	v_add_u32_e32 v21, 0xc14, v16
	v_add_u32_e32 v22, 0x1414, v16
	v_add_u32_e32 v23, 0x141c, v16
	v_add_u32_e32 v24, 0x1818, v16
	v_add_u32_e32 v25, 0x1c1c, v16
	v_add_u32_e32 v26, 0x1c24, v16
	v_lshlrev_b32_e32 v2, 1, v2
	v_add_u32_e32 v27, v7, v9
	v_lshlrev_b32_e32 v4, 1, v4
	v_lshlrev_b32_e32 v6, 1, v6
	v_lshlrev_b32_e32 v8, 1, v8
	v_lshlrev_b32_e32 v10, 1, v10
	s_branch .LBB0_2280

; __device__ __forceinline__ unsigned g8_cvt_pk(float lo, float hi) { unsigned r; asm volatile("v_cvt_pk_bf16_f32 %0, %1, %2" : "=v"(r) : "v"(lo), "v"(hi)); return r; }
; __device__ __forceinline__ void convert_deferred(const Ptrs& P, unsigned char* lds, int quota) {
;     ...
;         const int t = *slot;
;         if (t >= DEF_GU + DEF_DN) break;
;         const bool gu = t < DEF_GU;
;         const float* src = gu ? P.in[34] : P.in[36]; bf16* dst = (bf16*)(P.ws + (gu ? WS_WGU : WS_WDN));
;         const int N = gu ? 2048 : 1024, ntn = N / 256, it = gu ? 2 * NE * 16 * 8 - DEF_GU + t : 2 * NE * 16 * 4 - DEF_DN + (t - DEF_GU);
;         f32x4 cur[8];
;         bt_load(src, N, gu ? 1 : 0, it, ntn, cur);
; #pragma unroll
;         for (int i = 0; i < 8; ++i) { float* tp = tile + (wid * 8 + i) * 257 + lane * 4; tp[0] = cur[i][0]; tp[1] = cur[i][1]; tp[2] = cur[i][2]; tp[3] = cur[i][3]; }
;         __syncthreads();
;         const int per = 16 * ntn, z = it / per, r = it % per, kt = r / ntn, nt = r % ntn;
;         bf16* d = dst + (size_t)z * N * 1024 + (((size_t)nt * 16 + kt) << 14);
;         const int kc = lane & 7;
; #pragma unroll
;         for (int pss = 0; pss < 4; ++pss) {
;             const int nn = wid * 32 + pss * 8 + (lane >> 3); float f[8];
; #pragma unroll
;             for (int j = 0; j < 8; ++j) f[j] = tile[(kc * 8 + j) * 257 + nn];
;             u32x4 w; w.x = g8_cvt_pk(f[0], f[1]); w.y = g8_cvt_pk(f[2], f[3]); w.z = g8_cvt_pk(f[4], f[5]); w.w = g8_cvt_pk(f[6], f[7]);
;             *(u32x4*)(d + nn * 64 + kc * 8) = w;
;         }
.LBB0_2284:
	s_or_b64 exec, exec, s[4:5]
	s_waitcnt lgkmcnt(0)
	s_barrier
	ds_read_b32 v5, v15
	s_mov_b64 s[4:5], -1
	s_waitcnt lgkmcnt(0)
	v_cmp_lt_i32_e32 vcc, s11, v5
	v_readfirstlane_b32 s0, v5
	s_cbranch_vccnz .LBB0_2279
	s_cmpk_gt_i32 s0, 0xbb7
	s_cselect_b64 vcc, -1, 0
	s_and_b64 s[4:5], vcc, exec
	s_cselect_b32 s4, s13, 0x104e000
	s_cselect_b32 s9, 0x400, s12
	s_cselect_b32 s15, s73, s69
	s_cselect_b32 s18, s72, s68
	s_cselect_b32 s5, s14, 0x1448
	s_cselect_b32 s16, 20, 21
	s_cselect_b32 s19, 10, 11
	s_add_u32 s22, s78, s4
	s_addc_u32 s23, s79, 0
	s_lshr_b32 s6, s9, 4
	s_abs_i32 s4, s6
	v_cvt_f32_u32_e32 v5, s4
	s_sub_i32 s17, 0, s4
	s_add_i32 s5, s5, s0
	s_abs_i32 s7, s5
	v_rcp_iflag_f32_e32 v5, v5
	s_xor_b32 s0, s5, s6
	s_lshr_b32 s8, s9, 8
	s_ashr_i32 s0, s0, 31
	v_mul_f32_e32 v5, 0x4f7ffffe, v5
	v_cvt_u32_f32_e32 v5, v5
	s_nop 0
	v_readfirstlane_b32 s24, v5
	s_mul_i32 s17, s17, s24
	s_mul_hi_u32 s17, s24, s17
	s_add_i32 s24, s24, s17
	s_mul_hi_u32 s17, s7, s24
	s_mul_i32 s24, s17, s4
	s_sub_i32 s7, s7, s24
	s_add_i32 s24, s17, 1
	s_sub_i32 s25, s7, s4
	s_cmp_ge_u32 s7, s4
	s_cselect_b32 s17, s24, s17
	s_cselect_b32 s7, s25, s7
	s_add_i32 s24, s17, 1
	s_cmp_ge_u32 s7, s4
	s_cselect_b32 s4, s24, s17
	s_xor_b32 s4, s4, s0
	s_sub_i32 s4, s4, s0
	s_sext_i32_i8 s0, s8
	v_cvt_f32_i32_e32 v5, s0
	s_mul_i32 s6, s4, s6
	s_sub_i32 s5, s5, s6
	v_cvt_f32_i32_e32 v7, s5
	v_rcp_iflag_f32_e32 v9, v5
	s_xor_b32 s0, s5, s0
	s_ashr_i32 s0, s0, 30
	s_or_b32 s0, s0, 1
	v_mul_f32_e32 v9, v7, v9
	v_trunc_f32_e32 v9, v9
	v_fma_f32 v7, -v9, v5, v7
	v_cvt_i32_f32_e32 v9, v9
	v_cmp_ge_f32_e64 s[6:7], |v7|, |v5|
	s_and_b64 s[6:7], s[6:7], exec
	s_cselect_b32 s0, s0, 0
	v_readfirstlane_b32 s6, v9
	s_add_i32 s6, s6, s0
	s_mul_i32 s7, s6, s8
	s_sub_i32 s8, s5, s7
	s_sext_i32_i8 s5, s8
	v_lshl_add_u32 v5, s5, 7, v12
	v_lshl_or_b32 v7, s5, 8, v13
	s_ashr_i32 s5, s4, 31
	s_sext_i32_i8 s0, s6
	s_lshl_b64 s[16:17], s[4:5], s16
	v_lshl_or_b32 v30, s0, 6, v14
	s_lshl_b64 s[16:17], s[16:17], 2
	v_ashrrev_i32_e32 v31, 31, v30
	s_add_u32 s16, s18, s16
	v_cndmask_b32_e32 v28, v5, v7, vcc
	s_addc_u32 s17, s15, s17
	v_lshlrev_b64 v[30:31], s19, v[30:31]
	v_lshl_add_u64 v[30:31], v[30:31], 2, s[16:17]
	v_ashrrev_i32_e32 v29, 31, v28
	v_lshl_add_u64 v[52:53], v[28:29], 2, v[30:31]
	s_lshl_b32 s0, s9, 2
	s_lshl_b64 s[16:17], 12, s19
	v_lshl_add_u64 v[36:37], v[52:53], 0, s[0:1]
	v_lshl_add_u64 v[44:45], v[52:53], 0, s[16:17]
	s_lshl_b64 s[16:17], 24, s19
	v_lshl_add_u64 v[54:55], v[36:37], 0, s[0:1]
	v_lshl_add_u64 v[56:57], v[52:53], 0, s[16:17]
	s_lshl_b64 s[16:17], 28, s19
	s_lshl_b32 s0, s9, 3
	v_lshl_add_u64 v[58:59], v[52:53], 0, s[16:17]
	v_lshl_add_u64 v[60:61], v[54:55], 0, s[0:1]
	s_lshl_b64 s[16:17], 20, s19
	global_load_dwordx4 v[28:31], v[52:53], off nt
	global_load_dwordx4 v[32:35], v[36:37], off nt
	s_nop 0
	global_load_dwordx4 v[36:39], v[54:55], off nt
	global_load_dwordx4 v[40:43], v[44:45], off nt
	s_nop 0
	global_load_dwordx4 v[44:47], v[56:57], off nt
	global_load_dwordx4 v[48:51], v[58:59], off nt
	v_lshl_add_u64 v[62:63], v[52:53], 0, s[16:17]
	global_load_dwordx4 v[52:55], v[60:61], off nt
	global_load_dwordx4 v[56:59], v[62:63], off nt
	s_lshl_b64 s[4:5], s[4:5], s19
	s_lshl_b64 s[4:5], s[4:5], 11
	s_add_u32 s0, s22, s4
	s_addc_u32 s9, s23, s5
	s_bfe_i64 s[4:5], s[8:9], 0x80000
	s_bfe_i64 s[6:7], s[6:7], 0x80000
	s_lshl_b64 s[4:5], s[4:5], 19
	s_add_u32 s0, s0, s4
	s_addc_u32 s8, s9, s5
	s_lshl_b64 s[4:5], s[6:7], 15
	s_add_u32 s4, s0, s4
	s_addc_u32 s5, s8, s5
	v_mov_b32_e32 v5, v3
	s_add_i32 s3, s3, -1
	s_cmp_eq_u32 s3, 0
	s_waitcnt vmcnt(7)
	ds_write_b128 v16, v[28:31]
	s_waitcnt vmcnt(6)
	ds_write2_b32 v17, v32, v33 offset1:1
	ds_write2_b32 v18, v34, v35 offset1:1
	s_waitcnt vmcnt(3)
	ds_write2_b64 v24, v[44:45], v[46:47] offset1:1
	s_waitcnt vmcnt(2)
	ds_write2_b32 v25, v48, v49 offset1:1
	ds_write2_b32 v26, v50, v51 offset1:1
	ds_write2_b64 v19, v[36:37], v[38:39] offset1:1
	ds_write2_b32 v20, v40, v41 offset1:1
	ds_write2_b32 v21, v42, v43 offset1:1
	s_waitcnt vmcnt(1)
	ds_write_b128 v16, v[52:55] offset:4112
	s_waitcnt vmcnt(0)
	ds_write2_b32 v22, v56, v57 offset1:1
	ds_write2_b32 v23, v58, v59 offset1:1
	s_waitcnt lgkmcnt(0)
	s_barrier
	ds_read_b32 v7, v27 offset:1028
	ds_read_b32 v9, v27 offset:3084
	ds_read_b32 v11, v27 offset:5140
	ds_read_b32 v31, v27 offset:7196
	ds_read_b32 v32, v27 offset:6168
	ds_read_b32 v30, v27 offset:4112
	ds_read_b32 v29, v27 offset:2056
	ds_read_b32 v28, v27
	s_waitcnt lgkmcnt(0)
	v_cvt_pk_bf16_f32 v28, v28, v7
	v_cvt_pk_bf16_f32 v29, v29, v9
	v_cvt_pk_bf16_f32 v30, v30, v11
	v_cvt_pk_bf16_f32 v31, v32, v31
	ds_read_b32 v7, v27 offset:1060
	ds_read_b32 v9, v27 offset:3116
	ds_read_b32 v11, v27 offset:5172
	ds_read_b32 v36, v27 offset:7228
	ds_read_b32 v37, v27 offset:6200
	ds_read_b32 v38, v27 offset:4144
	ds_read_b32 v39, v27 offset:2088
	ds_read_b32 v40, v27 offset:32
	v_lshl_add_u64 v[32:33], s[4:5], 0, v[2:3]
	v_lshl_add_u64 v[34:35], v[32:33], 0, v[4:5]
	global_store_dwordx4 v[34:35], v[28:31], off
	s_cselect_b64 s[4:5], -1, 0
	s_waitcnt lgkmcnt(0)
	v_cvt_pk_bf16_f32 v28, v40, v7
	v_cvt_pk_bf16_f32 v29, v39, v9
	v_cvt_pk_bf16_f32 v30, v38, v11
	v_cvt_pk_bf16_f32 v31, v37, v36
	ds_read_b32 v5, v27 offset:1092
	ds_read_b32 v9, v27 offset:3148
	ds_read_b32 v11, v27 offset:5204
	ds_read_b32 v36, v27 offset:6232
	ds_read_b32 v37, v27 offset:4176
	ds_read_b32 v38, v27 offset:2120
	ds_read_b32 v39, v27 offset:64
	ds_read_b32 v40, v27 offset:7260
	v_mov_b32_e32 v7, v3
	v_lshl_add_u64 v[34:35], v[32:33], 0, v[6:7]
	global_store_dwordx4 v[34:35], v[28:31], off
	s_waitcnt lgkmcnt(1)
	s_nop 0
	v_cvt_pk_bf16_f32 v28, v39, v5
	v_cvt_pk_bf16_f32 v29, v38, v9
	v_cvt_pk_bf16_f32 v30, v37, v11
	s_waitcnt lgkmcnt(0)
	v_cvt_pk_bf16_f32 v31, v36, v40
	ds_read_b32 v5, v27 offset:1124
	ds_read_b32 v7, v27 offset:3180
	ds_read_b32 v11, v27 offset:5236
	ds_read_b32 v36, v27 offset:6264
	ds_read_b32 v37, v27 offset:4208
	ds_read_b32 v38, v27 offset:2152
	ds_read_b32 v39, v27 offset:96
	ds_read_b32 v40, v27 offset:7292
	v_mov_b32_e32 v9, v3
	v_lshl_add_u64 v[34:35], v[32:33], 0, v[8:9]
	global_store_dwordx4 v[34:35], v[28:31], off
	s_waitcnt lgkmcnt(1)
	s_nop 0
	v_cvt_pk_bf16_f32 v28, v39, v5
	v_cvt_pk_bf16_f32 v29, v38, v7
	v_cvt_pk_bf16_f32 v30, v37, v11
	v_mov_b32_e32 v11, v3
	v_lshl_add_u64 v[32:33], v[32:33], 0, v[10:11]
	s_waitcnt lgkmcnt(0)
	v_cvt_pk_bf16_f32 v31, v36, v40
	global_store_dwordx4 v[32:33], v[28:31], off
	s_branch .LBB0_2279
